# LN1/router: the per-group router weight batch is issued before the workgroup barrier that precedes the router products (its L2 latency overlaps the barrier wait)
# baseline (speedup 1.0000x reference)
; #define GAS __attribute__((address_space(1)))
; template <bool SKIP_MIX>
; __device__ __forceinline__ void p8_ln_router(Frame& F0, const In& I) {
;     ...
;         { f32x4 va[8], vb[8];
;           const size_t tokA = (size_t)(tok0 + 2 * w), tokB = tokA + 1;
;           const GAS f32x4* zra = (const GAS f32x4*)(zsrc + tokA * D) + lane; const GAS f32x4* zrb = (const GAS f32x4*)(zsrc + tokB * D) + lane;
;           const GAS v2u* mra = (const GAS v2u*)(mixb + tokA * D) + lane; const GAS v2u* mrb = (const GAS v2u*)(mixb + tokB * D) + lane;
;           v2u ma[8], mb[8];
; #pragma unroll
;           for (int j = 0; j < 8; ++j) { va[j] = zra[64 * j]; vb[j] = zrb[64 * j]; if (!SKIP_MIX) { ma[j] = mra[64 * j]; mb[j] = mrb[64 * j]; } }
; #pragma unroll
;           for (int j = 0; j < 8; ++j) { va[j] = va[j] * DN_ALPHA; vb[j] = vb[j] * DN_ALPHA;
;               if (!SKIP_MIX) { va[j] += (f32x4){bflo(ma[j].x), bfhi(ma[j].x), bflo(ma[j].y), bfhi(ma[j].y)}; vb[j] += (f32x4){bflo(mb[j].x), bfhi(mb[j].x), bflo(mb[j].y), bfhi(mb[j].y)}; } }
; #pragma unroll
;           for (int tt = 0; tt < 2; ++tt) {
;             const int tl = 2 * w + tt; const size_t tok = (size_t)(tok0 + tl);
;             f32x4 v[8]; float s = 0.f;
; #pragma unroll
;             for (int j = 0; j < 8; ++j) { v[j] = tt ? vb[j] : va[j]; s += (v[j].x + v[j].y) + (v[j].z + v[j].w); }
;             const float mean = wave_sum(s) * (1.f / D); float s2 = 0.f;
.LBB0_1514:
	s_lshl_b32 s23, s22, 4
	s_add_i32 s0, s23, s8
	s_ashr_i32 s1, s0, 31
	s_lshl_b64 s[16:17], s[0:1], 12
	s_lshl_b64 s[14:15], s[0:1], 11
	s_lshl_b64 s[0:1], s[0:1], 13
	v_lshl_add_u64 v[66:67], v[82:83], 0, s[16:17]
	v_lshl_add_u64 v[68:69], v[80:81], 0, s[0:1]
	global_load_dwordx2 v[106:107], v[66:67], off
	global_load_dwordx2 v[108:109], v[66:67], off offset:512
	global_load_dwordx2 v[110:111], v[66:67], off offset:1024
	s_or_b32 s0, s14, 0x800
	s_mov_b32 s1, s15
	global_load_dwordx4 v[70:73], v[68:69], off
	v_lshl_add_u64 v[112:113], s[0:1], 1, v[82:83]
	v_lshl_add_u64 v[114:115], s[0:1], 2, v[80:81]
	global_load_dwordx2 v[124:125], v[112:113], off
	global_load_dwordx4 v[90:93], v[68:69], off offset:1024
	global_load_dwordx2 v[126:127], v[112:113], off offset:512
	global_load_dwordx4 v[94:97], v[68:69], off offset:2048
	global_load_dwordx2 v[128:129], v[112:113], off offset:1024
	global_load_dwordx4 v[98:101], v[114:115], off
	global_load_dwordx4 v[102:105], v[114:115], off offset:1024
	global_load_dwordx4 v[116:119], v[114:115], off offset:2048
	global_load_dwordx2 v[142:143], v[66:67], off offset:1536
	global_load_dwordx4 v[120:123], v[68:69], off offset:3072
	global_load_dwordx2 v[144:145], v[112:113], off offset:1536
	global_load_dwordx4 v[130:133], v[114:115], off offset:3072
	global_load_dwordx2 v[184:185], v[66:67], off offset:2048
	v_add_co_u32_e32 v68, vcc, s19, v68
	s_waitcnt vmcnt(14)
	v_lshlrev_b32_e32 v198, 16, v110
	v_addc_co_u32_e32 v69, vcc, 0, v69, vcc
	global_load_dwordx4 v[134:137], v[68:69], off
	global_load_dwordx2 v[186:187], v[112:113], off offset:2048
	v_add_co_u32_e32 v138, vcc, s19, v114
	v_and_b32_e32 v199, 0xffff0000, v110
	s_nop 0
	v_addc_co_u32_e32 v139, vcc, 0, v115, vcc
	global_load_dwordx4 v[160:163], v[138:139], off
	global_load_dwordx2 v[188:189], v[66:67], off offset:2560
	global_load_dwordx4 v[164:167], v[68:69], off offset:1024
	global_load_dwordx2 v[190:191], v[112:113], off offset:2560
	global_load_dwordx4 v[168:171], v[138:139], off offset:1024
	global_load_dwordx2 v[192:193], v[66:67], off offset:3072
	global_load_dwordx2 v[194:195], v[66:67], off offset:3584
	global_load_dwordx4 v[172:175], v[68:69], off offset:2048
	global_load_dwordx4 v[176:179], v[68:69], off offset:3072
	global_load_dwordx2 v[196:197], v[112:113], off offset:3072
	global_load_dwordx2 v[114:115], v[112:113], off offset:3584
	global_load_dwordx4 v[180:183], v[138:139], off offset:2048
	s_nop 0
	global_load_dwordx4 v[66:69], v[138:139], off offset:3072
	v_lshlrev_b32_e32 v112, 16, v106
	v_and_b32_e32 v113, 0xffff0000, v106
	v_lshlrev_b32_e32 v106, 16, v107
	v_and_b32_e32 v107, 0xffff0000, v107
	v_lshlrev_b32_e32 v138, 16, v108
	v_and_b32_e32 v139, 0xffff0000, v108
	v_lshlrev_b32_e32 v108, 16, v109
	v_and_b32_e32 v109, 0xffff0000, v109
	v_lshlrev_b32_e32 v110, 16, v111
	v_and_b32_e32 v111, 0xffff0000, v111
	s_waitcnt vmcnt(28)
	v_pk_fma_f32 v[148:149], v[72:73], s[12:13], v[106:107] op_sel_hi:[1,0,1]
	v_pk_fma_f32 v[150:151], v[70:71], s[12:13], v[112:113] op_sel_hi:[1,0,1]
	s_waitcnt vmcnt(27)
	v_lshlrev_b32_e32 v70, 16, v124
	v_and_b32_e32 v71, 0xffff0000, v124
	v_lshlrev_b32_e32 v72, 16, v125
	v_and_b32_e32 v73, 0xffff0000, v125
	s_waitcnt vmcnt(26)
	v_pk_fma_f32 v[140:141], v[92:93], s[12:13], v[108:109] op_sel_hi:[1,0,1]
	v_pk_fma_f32 v[146:147], v[90:91], s[12:13], v[138:139] op_sel_hi:[1,0,1]
	s_waitcnt vmcnt(25)
	v_lshlrev_b32_e32 v90, 16, v126
	v_and_b32_e32 v91, 0xffff0000, v126
	v_lshlrev_b32_e32 v92, 16, v127
	v_and_b32_e32 v93, 0xffff0000, v127
	s_waitcnt vmcnt(24)
	v_pk_fma_f32 v[126:127], v[96:97], s[12:13], v[110:111] op_sel_hi:[1,0,1]
	s_waitcnt vmcnt(22)
	v_pk_fma_f32 v[110:111], v[100:101], s[12:13], v[72:73] op_sel_hi:[1,0,1]
	v_pk_fma_f32 v[112:113], v[98:99], s[12:13], v[70:71] op_sel_hi:[1,0,1]
	s_waitcnt vmcnt(19)
	v_lshlrev_b32_e32 v70, 16, v142
	v_and_b32_e32 v71, 0xffff0000, v142
	v_lshlrev_b32_e32 v72, 16, v143
	v_and_b32_e32 v73, 0xffff0000, v143
	v_pk_fma_f32 v[138:139], v[94:95], s[12:13], v[198:199] op_sel_hi:[1,0,1]
	v_lshlrev_b32_e32 v96, 16, v128
	v_and_b32_e32 v97, 0xffff0000, v128
	v_lshlrev_b32_e32 v94, 16, v129
	v_and_b32_e32 v95, 0xffff0000, v129
	s_waitcnt vmcnt(18)
	v_pk_fma_f32 v[128:129], v[122:123], s[12:13], v[72:73] op_sel_hi:[1,0,1]
	v_pk_fma_f32 v[142:143], v[120:121], s[12:13], v[70:71] op_sel_hi:[1,0,1]
	s_waitcnt vmcnt(17)
	v_lshlrev_b32_e32 v70, 16, v144
	v_and_b32_e32 v71, 0xffff0000, v144
	v_lshlrev_b32_e32 v72, 16, v145
	v_and_b32_e32 v73, 0xffff0000, v145
	v_pk_fma_f32 v[106:107], v[104:105], s[12:13], v[92:93] op_sel_hi:[1,0,1]
	v_pk_fma_f32 v[108:109], v[102:103], s[12:13], v[90:91] op_sel_hi:[1,0,1]
	v_pk_fma_f32 v[104:105], v[116:117], s[12:13], v[96:97] op_sel_hi:[1,0,1]
	s_waitcnt vmcnt(16)
	v_pk_fma_f32 v[92:93], v[132:133], s[12:13], v[72:73] op_sel_hi:[1,0,1]
	v_pk_fma_f32 v[102:103], v[130:131], s[12:13], v[70:71] op_sel_hi:[1,0,1]
	s_waitcnt vmcnt(15)
	v_lshlrev_b32_e32 v70, 16, v184
	v_and_b32_e32 v71, 0xffff0000, v184
	v_lshlrev_b32_e32 v72, 16, v185
	v_and_b32_e32 v73, 0xffff0000, v185
	v_mov_b32_e32 v144, v151
	v_mov_b32_e32 v145, v147
	v_pk_fma_f32 v[94:95], v[118:119], s[12:13], v[94:95] op_sel_hi:[1,0,1]
	s_waitcnt vmcnt(11)
	v_lshlrev_b32_e32 v90, 16, v189
	v_and_b32_e32 v91, 0xffff0000, v189
	s_waitcnt vmcnt(10)
	v_pk_fma_f32 v[124:125], v[166:167], s[12:13], v[90:91] op_sel_hi:[1,0,1]
	s_waitcnt vmcnt(9)
	v_lshlrev_b32_e32 v90, 16, v191
	v_pk_fma_f32 v[122:123], v[136:137], s[12:13], v[72:73] op_sel_hi:[1,0,1]
	s_waitcnt vmcnt(6)
; template <bool SKIP_MIX>
; __device__ __forceinline__ void p8_ln_router(Frame& F0, const In& I) {
;     ...
;             f32x4 v[8]; float s = 0.f;
; #pragma unroll
;             for (int j = 0; j < 8; ++j) { v[j] = tt ? vb[j] : va[j]; s += (v[j].x + v[j].y) + (v[j].z + v[j].w); }
;             const float mean = wave_sum(s) * (1.f / D); float s2 = 0.f;
; #pragma unroll
;             for (int j = 0; j < 8; ++j) { v[j] = v[j] - mean; s2 += (v[j].x * v[j].x + v[j].y * v[j].y) + (v[j].z * v[j].z + v[j].w * v[j].w); }
	v_lshlrev_b32_e32 v116, 16, v194
	v_and_b32_e32 v117, 0xffff0000, v194
	v_pk_fma_f32 v[136:137], v[134:135], s[12:13], v[70:71] op_sel_hi:[1,0,1]
	v_lshlrev_b32_e32 v70, 16, v186
	v_and_b32_e32 v71, 0xffff0000, v186
	s_waitcnt vmcnt(4)
	v_pk_fma_f32 v[132:133], v[176:177], s[12:13], v[116:117] op_sel_hi:[1,0,1]
	v_mov_b32_e32 v116, v150
	v_mov_b32_e32 v117, v146
	v_pk_fma_f32 v[100:101], v[160:161], s[12:13], v[70:71] op_sel_hi:[1,0,1]
	v_pk_add_f32 v[116:117], v[116:117], v[144:145]
	v_mov_b32_e32 v144, v148
	v_mov_b32_e32 v145, v140
	v_mov_b32_e32 v160, v149
	v_mov_b32_e32 v161, v141
	v_pk_add_f32 v[144:145], v[144:145], v[160:161]
	v_mov_b32_e32 v160, v138
	v_pk_add_f32 v[116:117], v[116:117], v[144:145]
	v_pk_mov_b32 v[144:145], v[138:139], v[126:127] op_sel:[1,0]
	v_mov_b32_e32 v161, v127
	v_pk_add_f32 v[144:145], v[144:145], v[160:161]
	v_lshlrev_b32_e32 v72, 16, v187
	v_and_b32_e32 v73, 0xffff0000, v187
	v_add_f32_e32 v116, 0, v116
	v_pk_add_f32 v[144:145], v[144:145], v[144:145] op_sel:[0,1] op_sel_hi:[1,0]
	v_pk_fma_f32 v[72:73], v[162:163], s[12:13], v[72:73] op_sel_hi:[1,0,1]
	v_lshlrev_b32_e32 v70, 16, v188
	v_and_b32_e32 v71, 0xffff0000, v188
	v_add_f32_e32 v116, v116, v117
	v_add_f32_e32 v160, v142, v143
	v_add_f32_e32 v162, v128, v129
	v_mov_b32_e32 v117, v136
	v_mov_b32_e32 v145, v137
	v_mov_b32_e32 v161, v122
	v_mov_b32_e32 v163, v123
	v_pk_fma_f32 v[130:131], v[164:165], s[12:13], v[70:71] op_sel_hi:[1,0,1]
	v_pk_add_f32 v[116:117], v[116:117], v[144:145]
	v_pk_add_f32 v[144:145], v[160:161], v[162:163]
	v_lshlrev_b32_e32 v70, 16, v190
	v_and_b32_e32 v71, 0xffff0000, v190
	v_pk_add_f32 v[116:117], v[116:117], v[144:145]
	v_pk_mov_b32 v[144:145], v[130:131], v[124:125] op_sel:[1,0]
	v_mov_b32_e32 v160, v130
	v_mov_b32_e32 v161, v125
	v_pk_fma_f32 v[96:97], v[168:169], s[12:13], v[70:71] op_sel_hi:[1,0,1]
	v_lshlrev_b32_e32 v70, 16, v192
	v_and_b32_e32 v71, 0xffff0000, v192
	v_lshlrev_b32_e32 v98, 16, v193
	v_and_b32_e32 v99, 0xffff0000, v193
	v_lshlrev_b32_e32 v118, 16, v195
	v_and_b32_e32 v119, 0xffff0000, v195
	v_pk_add_f32 v[144:145], v[144:145], v[160:161]
	v_pk_fma_f32 v[120:121], v[174:175], s[12:13], v[98:99] op_sel_hi:[1,0,1]
	v_pk_fma_f32 v[134:135], v[172:173], s[12:13], v[70:71] op_sel_hi:[1,0,1]
	v_pk_fma_f32 v[118:119], v[178:179], s[12:13], v[118:119] op_sel_hi:[1,0,1]
	v_pk_add_f32 v[116:117], v[116:117], v[116:117] op_sel:[0,1] op_sel_hi:[1,0]
	v_pk_add_f32 v[144:145], v[144:145], v[144:145] op_sel:[0,1] op_sel_hi:[1,0]
	v_add_f32_e32 v160, v134, v135
	v_add_f32_e32 v162, v120, v121
	v_mov_b32_e32 v117, v132
	v_mov_b32_e32 v145, v133
	v_mov_b32_e32 v161, v118
	v_mov_b32_e32 v163, v119
	v_pk_add_f32 v[116:117], v[116:117], v[144:145]
	v_pk_add_f32 v[144:145], v[160:161], v[162:163]
	v_and_b32_e32 v91, 0xffff0000, v191
	v_pk_add_f32 v[116:117], v[116:117], v[144:145]
	v_pk_fma_f32 v[90:91], v[170:171], s[12:13], v[90:91] op_sel_hi:[1,0,1]
	v_add_f32_e32 v116, v116, v117
	s_waitcnt vmcnt(3)
	v_lshlrev_b32_e32 v98, 16, v196
	v_and_b32_e32 v99, 0xffff0000, v196
	v_add_f32_dpp v116, v116, v116 quad_perm:[1,0,3,2] row_mask:0xf bank_mask:0xf bound_ctrl:1
	v_lshlrev_b32_e32 v70, 16, v197
	v_and_b32_e32 v71, 0xffff0000, v197
	v_add_f32_dpp v116, v116, v116 quad_perm:[2,3,0,1] row_mask:0xf bank_mask:0xf bound_ctrl:1
	s_waitcnt vmcnt(1)
	v_pk_fma_f32 v[70:71], v[182:183], s[12:13], v[70:71] op_sel_hi:[1,0,1]
	v_pk_fma_f32 v[98:99], v[180:181], s[12:13], v[98:99] op_sel_hi:[1,0,1]
	v_add_f32_dpp v116, v116, v116 row_ror:4 row_mask:0xf bank_mask:0xf bound_ctrl:1
	s_nop 1
	v_add_f32_dpp v116, v116, v116 row_ror:8 row_mask:0xf bank_mask:0xf bound_ctrl:1
	s_nop 0
	v_readlane_b32 s24, v116, 16
	v_readlane_b32 s25, v116, 48
	v_readlane_b32 s0, v116, 0
	v_readlane_b32 s1, v116, 32
	v_mov_b32_e32 v116, s24
	v_mov_b32_e32 v117, s25
	v_pk_add_f32 v[116:117], s[0:1], v[116:117]
	s_nop 0
	v_add_f32_e32 v164, v116, v117
	v_fmamk_f32 v151, v164, 0xba000000, v151
	v_fmamk_f32 v147, v164, 0xba000000, v147
	v_fmamk_f32 v149, v164, 0xba000000, v149
	v_fmac_f32_e32 v150, 0xba000000, v164
	v_fmamk_f32 v141, v164, 0xba000000, v141
	v_fmac_f32_e32 v146, 0xba000000, v164
	v_mov_b32_e32 v144, v151
	v_mov_b32_e32 v145, v147
	v_fmac_f32_e32 v148, 0xba000000, v164
	v_fmac_f32_e32 v140, 0xba000000, v164
	v_mov_b32_e32 v116, v150
	v_mov_b32_e32 v117, v146
	v_pk_mul_f32 v[144:145], v[144:145], v[144:145]
	v_mov_b32_e32 v160, v149
	v_mov_b32_e32 v161, v141
	v_pk_fma_f32 v[116:117], v[116:117], v[116:117], v[144:145]
	v_mov_b32_e32 v144, v148
	v_mov_b32_e32 v145, v140
	v_pk_mul_f32 v[160:161], v[160:161], v[160:161]
	v_fmamk_f32 v139, v164, 0xba000000, v139
	v_pk_fma_f32 v[144:145], v[144:145], v[144:145], v[160:161]
	v_fmac_f32_e32 v138, 0xba000000, v164
	v_pk_add_f32 v[116:117], v[116:117], v[144:145]
	v_fmamk_f32 v127, v164, 0xba000000, v127
	v_fmac_f32_e32 v126, 0xba000000, v164
	v_pk_add_f32 v[116:117], v[116:117], v[116:117] op_sel_hi:[0,1]
	v_pk_mul_f32 v[144:145], v[126:127], v[126:127]
	v_pk_mul_f32 v[160:161], v[138:139], v[138:139]
	v_fmac_f32_e32 v142, 0xba000000, v164
	v_pk_mov_b32 v[162:163], v[160:161], v[144:145] op_sel:[1,0]
	v_mov_b32_e32 v161, v145
	v_fmac_f32_e32 v128, 0xba000000, v164
	v_fmamk_f32 v143, v164, 0xba000000, v143
	v_mul_f32_e32 v116, v142, v142
	v_pk_add_f32 v[144:145], v[162:163], v[160:161]
	v_fmamk_f32 v129, v164, 0xba000000, v129
	v_pk_fma_f32 v[160:161], v[142:143], v[142:143], v[116:117] op_sel_hi:[1,1,0]
	v_mul_f32_e32 v116, v128, v128
	v_pk_add_f32 v[144:145], v[144:145], v[144:145] op_sel_hi:[0,1]
	v_pk_fma_f32 v[162:163], v[128:129], v[128:129], v[116:117] op_sel_hi:[1,1,0]
	v_fmamk_f32 v123, v164, 0xba000000, v123
; #define GAS __attribute__((address_space(1)))
; #define LAS __attribute__((address_space(3)))
; __device__ __forceinline__ unsigned cvt_pk_bf16(float lo, float hi) { const f32x2_t_ v = {lo, hi}; const bf16x2_t_ b = __builtin_convertvector(v, bf16x2_t_); return __builtin_bit_cast(unsigned, b); }
; template <bool SKIP_MIX>
; __device__ __forceinline__ void p8_ln_router(Frame& F0, const In& I) {
;     ...
;             for (int j = 0; j < 8; ++j) { v[j] = v[j] - mean; s2 += (v[j].x * v[j].x + v[j].y * v[j].y) + (v[j].z * v[j].z + v[j].w * v[j].w); }
;             const float rstd = 1.f / sqrtf(wave_sum(s2) * (1.f / D) + LN_EPS);
;             GAS v2u* h1 = (GAS v2u*)((bf16*)(F.ws + WS_H1) + tok * D) + lane;
;             GAS unsigned* h1b = (GAS unsigned*)((unsigned char*)(F.ws + WS_H1B) + tok * D) + lane;
; #pragma unroll
;             for (int j = 0; j < 8; ++j) { f32x4 h;
; #pragma unroll
;                 for (int e = 0; e < 4; ++e) h[e] = v[j][e] * rstd * ln_w[4 * j + e] + ln_b[4 * j + e];
;                 h1[64 * j] = (v2u){pg8::cvt_pk_bf16(h.x, h.y), pg8::cvt_pk_bf16(h.z, h.w)}; { int w8 = __builtin_amdgcn_cvt_pk_fp8_f32(h.x, h.y, 0, false); w8 = __builtin_amdgcn_cvt_pk_fp8_f32(h.z, h.w, w8, true); h1b[64 * j] = (unsigned)w8; }
;                 *(LAS f32x4*)(hs + tl * P8_PITCH + 4 * lane + 256 * j) = h; }
	v_fmac_f32_e32 v122, 0xba000000, v164
	v_fmamk_f32 v137, v164, 0xba000000, v137
	v_fmac_f32_e32 v136, 0xba000000, v164
	v_mul_f32_e32 v160, v136, v136
	v_mul_f32_e32 v162, v137, v137
	v_mul_f32_e32 v144, v122, v122
	v_mul_f32_e32 v116, v123, v123
	v_pk_add_f32 v[160:161], v[160:161], v[162:163]
	v_pk_add_f32 v[116:117], v[144:145], v[116:117]
	v_fmamk_f32 v131, v164, 0xba000000, v131
	v_pk_add_f32 v[116:117], v[160:161], v[116:117]
	v_fmac_f32_e32 v130, 0xba000000, v164
	v_fmamk_f32 v125, v164, 0xba000000, v125
	v_fmac_f32_e32 v124, 0xba000000, v164
	v_pk_add_f32 v[116:117], v[116:117], v[116:117] op_sel_hi:[0,1]
	v_pk_mul_f32 v[144:145], v[124:125], v[124:125]
	v_pk_mul_f32 v[160:161], v[130:131], v[130:131]
	v_fmac_f32_e32 v134, 0xba000000, v164
	v_pk_mov_b32 v[162:163], v[160:161], v[144:145] op_sel:[1,0]
	v_mov_b32_e32 v161, v145
	v_fmac_f32_e32 v120, 0xba000000, v164
	v_fmamk_f32 v135, v164, 0xba000000, v135
	v_mul_f32_e32 v116, v134, v134
	v_pk_add_f32 v[144:145], v[162:163], v[160:161]
	v_fmamk_f32 v121, v164, 0xba000000, v121
	v_pk_fma_f32 v[160:161], v[134:135], v[134:135], v[116:117] op_sel_hi:[1,1,0]
	v_mul_f32_e32 v116, v120, v120
	v_pk_add_f32 v[144:145], v[144:145], v[144:145] op_sel_hi:[0,1]
	v_pk_fma_f32 v[162:163], v[120:121], v[120:121], v[116:117] op_sel_hi:[1,1,0]
	v_fmamk_f32 v119, v164, 0xba000000, v119
	v_fmac_f32_e32 v118, 0xba000000, v164
	v_fmamk_f32 v133, v164, 0xba000000, v133
	v_fmac_f32_e32 v132, 0xba000000, v164
	v_mul_f32_e32 v160, v132, v132
	v_mul_f32_e32 v162, v133, v133
	v_mul_f32_e32 v144, v118, v118
	v_mul_f32_e32 v116, v119, v119
	v_pk_add_f32 v[160:161], v[160:161], v[162:163]
	v_pk_add_f32 v[116:117], v[144:145], v[116:117]
	v_mov_b32_e32 v162, 0
	v_pk_add_f32 v[116:117], v[160:161], v[116:117]
	s_nop 0
	v_add_f32_e32 v116, v116, v117
	s_nop 1
	v_add_f32_dpp v116, v116, v116 quad_perm:[1,0,3,2] row_mask:0xf bank_mask:0xf bound_ctrl:1
	s_nop 1
	v_add_f32_dpp v116, v116, v116 quad_perm:[2,3,0,1] row_mask:0xf bank_mask:0xf bound_ctrl:1
	s_nop 1
	v_add_f32_dpp v116, v116, v116 row_ror:4 row_mask:0xf bank_mask:0xf bound_ctrl:1
	s_nop 1
	v_add_f32_dpp v116, v116, v116 row_ror:8 row_mask:0xf bank_mask:0xf bound_ctrl:1
	s_nop 0
	v_readlane_b32 s24, v116, 16
	v_readlane_b32 s25, v116, 48
	v_readlane_b32 s0, v116, 0
	v_readlane_b32 s1, v116, 32
	v_mov_b32_e32 v116, s24
	v_mov_b32_e32 v117, s25
	v_pk_add_f32 v[116:117], s[0:1], v[116:117]
	s_nop 0
	v_add_f32_e32 v116, v116, v117
	v_fmamk_f32 v116, v116, 0x3a000000, v76
	v_mul_f32_e32 v117, 0x4f800000, v116
	v_cmp_gt_f32_e32 vcc, s20, v116
	s_nop 1
	v_cndmask_b32_e32 v144, v116, v117, vcc
	v_sqrt_f32_e32 v145, v144
	v_lshlrev_b32_e32 v116, 16, v114
	v_and_b32_e32 v117, 0xffff0000, v114
	s_waitcnt vmcnt(0)
	v_pk_fma_f32 v[116:117], v[66:67], s[12:13], v[116:117] op_sel_hi:[1,0,1]
	v_add_u32_e32 v160, -1, v145
	v_fma_f32 v161, -v160, v145, v144
	v_cmp_ge_f32_e64 s[0:1], 0, v161
	v_add_u32_e32 v161, 1, v145
	v_lshlrev_b32_e32 v114, 16, v115
	v_cndmask_b32_e64 v160, v145, v160, s[0:1]
	v_fma_f32 v145, -v161, v145, v144
	v_cmp_lt_f32_e64 s[0:1], 0, v145
	v_and_b32_e32 v115, 0xffff0000, v115
	v_pk_fma_f32 v[114:115], v[68:69], s[12:13], v[114:115] op_sel_hi:[1,0,1]
	v_cndmask_b32_e64 v145, v160, v161, s[0:1]
	v_mul_f32_e32 v160, 0x37800000, v145
	v_cndmask_b32_e32 v145, v145, v160, vcc
	v_cmp_class_f32_e32 vcc, v144, v155
	s_nop 1
	v_cndmask_b32_e32 v144, v145, v144, vcc
	v_div_scale_f32 v145, s[0:1], v144, v144, 1.0
	v_rcp_f32_e32 v160, v145
	s_nop 0
	v_fma_f32 v66, -v145, v160, 1.0
	v_fmac_f32_e32 v160, v66, v160
	v_div_scale_f32 v66, vcc, 1.0, v144, 1.0
	v_mul_f32_e32 v67, v66, v160
	v_fma_f32 v68, -v145, v67, v66
	v_fmac_f32_e32 v67, v68, v160
	v_fma_f32 v66, -v145, v67, v66
	v_div_fmas_f32 v66, v66, v160, v67
	v_div_fixup_f32 v160, v66, v144, 1.0
	v_pk_mul_f32 v[66:67], v[150:151], v[160:161] op_sel_hi:[1,0]
	v_mov_b32_e32 v161, 0
	v_pk_fma_f32 v[66:67], v[2:3], v[66:67], v[6:7]
	v_lshl_add_u64 v[144:145], v[84:85], 0, s[16:17]
	v_cvt_pk_fp8_f32 v161, v66, v67
	v_lshl_add_u64 v[150:151], v[86:87], 0, s[14:15]
	v_pk_mul_f32 v[68:69], v[148:149], v[160:161] op_sel_hi:[1,0]
	s_nop 0
	v_pk_fma_f32 v[68:69], v[4:5], v[68:69], v[8:9]
	v_cvt_pk_bf16_f32 v148, v66, v67
	v_cvt_pk_fp8_f32 v161, v68, v69 op_sel:[0,0,1]
	v_cvt_pk_bf16_f32 v149, v68, v69
	global_store_dwordx2 v[144:145], v[148:149], off
	global_store_dword v[150:151], v161, off
	v_add_u32_e32 v161, s9, v75
	v_pk_mul_f32 v[146:147], v[146:147], v[160:161] op_sel_hi:[1,0]
	ds_write_b128 v161, v[66:69]
	v_pk_fma_f32 v[146:147], v[10:11], v[146:147], v[14:15]
	v_pk_mul_f32 v[66:67], v[140:141], v[160:161] op_sel_hi:[1,0]
	v_cvt_pk_fp8_f32 v162, v146, v147
	v_pk_fma_f32 v[148:149], v[12:13], v[66:67], v[16:17]
	v_cvt_pk_bf16_f32 v66, v146, v147
	v_cvt_pk_bf16_f32 v67, v148, v149
	v_cvt_pk_fp8_f32 v162, v148, v149 op_sel:[0,0,1]
	global_store_dwordx2 v[144:145], v[66:67], off offset:512
	global_store_dword v[150:151], v162, off offset:256
	v_pk_mul_f32 v[66:67], v[138:139], v[160:161] op_sel_hi:[1,0]
	v_mov_b32_e32 v138, 0
	v_pk_fma_f32 v[66:67], v[18:19], v[66:67], v[22:23]
	v_pk_mul_f32 v[68:69], v[126:127], v[160:161] op_sel_hi:[1,0]
	v_cvt_pk_fp8_f32 v138, v66, v67
	v_pk_fma_f32 v[68:69], v[20:21], v[68:69], v[24:25]
	v_cvt_pk_bf16_f32 v126, v66, v67
	v_cvt_pk_bf16_f32 v127, v68, v69
	v_cvt_pk_fp8_f32 v138, v68, v69 op_sel:[0,0,1]
	ds_write_b128 v161, v[146:149] offset:1024
	global_store_dwordx2 v[144:145], v[126:127], off offset:1024
	global_store_dword v[150:151], v138, off offset:512
	v_pk_mul_f32 v[126:127], v[142:143], v[160:161] op_sel_hi:[1,0]
	v_mov_b32_e32 v138, 0
	v_pk_fma_f32 v[126:127], v[26:27], v[126:127], v[30:31]
; #define GAS __attribute__((address_space(1)))
; #define LAS __attribute__((address_space(3)))
; __device__ __forceinline__ unsigned cvt_pk_bf16(float lo, float hi) { const f32x2_t_ v = {lo, hi}; const bf16x2_t_ b = __builtin_convertvector(v, bf16x2_t_); return __builtin_bit_cast(unsigned, b); }
; template <bool SKIP_MIX>
; __device__ __forceinline__ void p8_ln_router(Frame& F0, const In& I) {
;     ...
;           for (int tt = 0; tt < 2; ++tt) {
;             const int tl = 2 * w + tt; const size_t tok = (size_t)(tok0 + tl);
;             f32x4 v[8]; float s = 0.f;
; #pragma unroll
;             for (int j = 0; j < 8; ++j) { v[j] = tt ? vb[j] : va[j]; s += (v[j].x + v[j].y) + (v[j].z + v[j].w); }
;             const float mean = wave_sum(s) * (1.f / D); float s2 = 0.f;
; #pragma unroll
;             for (int j = 0; j < 8; ++j) { v[j] = v[j] - mean; s2 += (v[j].x * v[j].x + v[j].y * v[j].y) + (v[j].z * v[j].z + v[j].w * v[j].w); }
;             const float rstd = 1.f / sqrtf(wave_sum(s2) * (1.f / D) + LN_EPS);
;             GAS v2u* h1 = (GAS v2u*)((bf16*)(F.ws + WS_H1) + tok * D) + lane;
;             GAS unsigned* h1b = (GAS unsigned*)((unsigned char*)(F.ws + WS_H1B) + tok * D) + lane;
; #pragma unroll
;             for (int j = 0; j < 8; ++j) { f32x4 h;
; #pragma unroll
;                 for (int e = 0; e < 4; ++e) h[e] = v[j][e] * rstd * ln_w[4 * j + e] + ln_b[4 * j + e];
;                 h1[64 * j] = (v2u){pg8::cvt_pk_bf16(h.x, h.y), pg8::cvt_pk_bf16(h.z, h.w)}; { int w8 = __builtin_amdgcn_cvt_pk_fp8_f32(h.x, h.y, 0, false); w8 = __builtin_amdgcn_cvt_pk_fp8_f32(h.z, h.w, w8, true); h1b[64 * j] = (unsigned)w8; }
;                 *(LAS f32x4*)(hs + tl * P8_PITCH + 4 * lane + 256 * j) = h; }
	ds_write_b128 v161, v[66:69] offset:2048
	v_cvt_pk_fp8_f32 v138, v126, v127
	v_pk_mul_f32 v[66:67], v[128:129], v[160:161] op_sel_hi:[1,0]
	v_pk_mul_f32 v[68:69], v[122:123], v[160:161] op_sel_hi:[1,0]
	v_pk_fma_f32 v[128:129], v[28:29], v[66:67], v[32:33]
	v_cvt_pk_bf16_f32 v66, v126, v127
	v_cvt_pk_fp8_f32 v138, v128, v129 op_sel:[0,0,1]
	v_cvt_pk_bf16_f32 v67, v128, v129
	global_store_dwordx2 v[144:145], v[66:67], off offset:1536
	global_store_dword v[150:151], v138, off offset:768
	v_pk_mul_f32 v[66:67], v[136:137], v[160:161] op_sel_hi:[1,0]
	v_mov_b32_e32 v136, 0
	v_pk_fma_f32 v[66:67], v[34:35], v[66:67], v[42:43]
	v_pk_fma_f32 v[68:69], v[36:37], v[68:69], v[44:45]
	v_cvt_pk_fp8_f32 v136, v66, v67
	v_cvt_pk_bf16_f32 v122, v66, v67
	v_cvt_pk_bf16_f32 v123, v68, v69
	ds_write_b128 v161, v[126:129] offset:3072
	v_cvt_pk_fp8_f32 v136, v68, v69 op_sel:[0,0,1]
	global_store_dwordx2 v[144:145], v[122:123], off offset:2048
	global_store_dword v[150:151], v136, off offset:1024
	v_pk_mul_f32 v[122:123], v[130:131], v[160:161] op_sel_hi:[1,0]
	v_mov_b32_e32 v126, 0
	v_pk_fma_f32 v[122:123], v[38:39], v[122:123], v[46:47]
	ds_write_b128 v161, v[66:69] offset:4096
	v_cvt_pk_fp8_f32 v126, v122, v123
	v_pk_mul_f32 v[66:67], v[124:125], v[160:161] op_sel_hi:[1,0]
	v_pk_mul_f32 v[68:69], v[120:121], v[160:161] op_sel_hi:[1,0]
	v_pk_fma_f32 v[124:125], v[40:41], v[66:67], v[48:49]
	v_cvt_pk_bf16_f32 v66, v122, v123
	v_cvt_pk_fp8_f32 v126, v124, v125 op_sel:[0,0,1]
	v_cvt_pk_bf16_f32 v67, v124, v125
	global_store_dwordx2 v[144:145], v[66:67], off offset:2560
	global_store_dword v[150:151], v126, off offset:1280
	v_pk_mul_f32 v[66:67], v[134:135], v[160:161] op_sel_hi:[1,0]
	v_mov_b32_e32 v126, 0
	v_pk_fma_f32 v[66:67], v[50:51], v[66:67], v[58:59]
	v_pk_fma_f32 v[68:69], v[52:53], v[68:69], v[60:61]
	v_cvt_pk_fp8_f32 v126, v66, v67
	v_cvt_pk_bf16_f32 v120, v66, v67
	v_cvt_pk_bf16_f32 v121, v68, v69
	ds_write_b128 v161, v[122:125] offset:5120
	v_cvt_pk_fp8_f32 v126, v68, v69 op_sel:[0,0,1]
	global_store_dwordx2 v[144:145], v[120:121], off offset:3072
	global_store_dword v[150:151], v126, off offset:1536
	v_mov_b32_e32 v120, v112
	v_mov_b32_e32 v121, v108
	v_mov_b32_e32 v122, v113
	v_mov_b32_e32 v123, v109
	v_pk_add_f32 v[120:121], v[120:121], v[122:123]
	v_mov_b32_e32 v122, v110
	v_mov_b32_e32 v123, v106
	v_mov_b32_e32 v124, v111
	v_mov_b32_e32 v125, v107
	v_pk_add_f32 v[122:123], v[122:123], v[124:125]
	v_mov_b32_e32 v124, v104
	v_pk_add_f32 v[120:121], v[120:121], v[122:123]
	v_pk_mov_b32 v[122:123], v[104:105], v[94:95] op_sel:[1,0]
	v_mov_b32_e32 v125, v95
	v_pk_add_f32 v[122:123], v[122:123], v[124:125]
	ds_write_b128 v161, v[66:69] offset:6144
	v_pk_mul_f32 v[68:69], v[118:119], v[160:161] op_sel_hi:[1,0]
	v_add_f32_e32 v119, 0, v120
	v_pk_add_f32 v[122:123], v[122:123], v[122:123] op_sel:[0,1] op_sel_hi:[1,0]
	v_add_f32_e32 v120, v119, v121
	v_add_f32_e32 v124, v102, v103
	v_add_f32_e32 v126, v92, v93
	v_mov_b32_e32 v121, v100
	v_mov_b32_e32 v123, v101
	v_mov_b32_e32 v125, v72
	v_mov_b32_e32 v127, v73
	v_pk_add_f32 v[120:121], v[120:121], v[122:123]
	v_pk_add_f32 v[122:123], v[124:125], v[126:127]
	v_mov_b32_e32 v124, v96
	v_pk_add_f32 v[120:121], v[120:121], v[122:123]
	v_pk_mov_b32 v[122:123], v[96:97], v[90:91] op_sel:[1,0]
	v_mov_b32_e32 v125, v91
	v_pk_add_f32 v[122:123], v[122:123], v[124:125]
	v_pk_add_f32 v[120:121], v[120:121], v[120:121] op_sel:[0,1] op_sel_hi:[1,0]
	v_pk_add_f32 v[122:123], v[122:123], v[122:123] op_sel:[0,1] op_sel_hi:[1,0]
	v_add_f32_e32 v124, v98, v99
	v_add_f32_e32 v126, v70, v71
	v_mov_b32_e32 v121, v116
	v_mov_b32_e32 v123, v117
	v_mov_b32_e32 v125, v114
	v_mov_b32_e32 v127, v115
	v_pk_add_f32 v[120:121], v[120:121], v[122:123]
	v_pk_add_f32 v[122:123], v[124:125], v[126:127]
	v_pk_mul_f32 v[66:67], v[132:133], v[160:161] op_sel_hi:[1,0]
	v_pk_add_f32 v[120:121], v[120:121], v[122:123]
	v_pk_fma_f32 v[66:67], v[54:55], v[66:67], v[62:63]
	v_add_f32_e32 v119, v120, v121
	v_mov_b32_e32 v128, 0
	v_cvt_pk_fp8_f32 v128, v66, v67
	v_add_f32_dpp v119, v119, v119 quad_perm:[1,0,3,2] row_mask:0xf bank_mask:0xf bound_ctrl:1
	v_pk_fma_f32 v[68:69], v[56:57], v[68:69], v[64:65]
	v_cvt_pk_bf16_f32 v118, v66, v67
	v_add_f32_dpp v119, v119, v119 quad_perm:[2,3,0,1] row_mask:0xf bank_mask:0xf bound_ctrl:1
	v_cvt_pk_fp8_f32 v128, v68, v69 op_sel:[0,0,1]
	s_nop 0
	v_add_f32_dpp v119, v119, v119 row_ror:4 row_mask:0xf bank_mask:0xf bound_ctrl:1
	s_nop 1
	v_add_f32_dpp v119, v119, v119 row_ror:8 row_mask:0xf bank_mask:0xf bound_ctrl:1
	s_nop 0
	v_readlane_b32 s14, v119, 16
	v_readlane_b32 s15, v119, 48
	v_readlane_b32 s0, v119, 0
	v_readlane_b32 s1, v119, 32
	v_mov_b32_e32 v120, s14
	v_mov_b32_e32 v121, s15
	v_pk_add_f32 v[120:121], s[0:1], v[120:121]
	s_nop 0
	v_add_f32_e32 v119, v120, v121
	v_fmamk_f32 v113, v119, 0xba000000, v113
	v_fmamk_f32 v109, v119, 0xba000000, v109
	v_fmamk_f32 v111, v119, 0xba000000, v111
	v_fmac_f32_e32 v112, 0xba000000, v119
	v_fmamk_f32 v107, v119, 0xba000000, v107
	v_fmac_f32_e32 v108, 0xba000000, v119
	v_mov_b32_e32 v122, v113
	v_mov_b32_e32 v123, v109
	v_fmac_f32_e32 v110, 0xba000000, v119
	v_fmac_f32_e32 v106, 0xba000000, v119
	v_mov_b32_e32 v120, v112
	v_mov_b32_e32 v121, v108
	v_pk_mul_f32 v[122:123], v[122:123], v[122:123]
	v_mov_b32_e32 v124, v111
	v_mov_b32_e32 v125, v107
	v_pk_fma_f32 v[120:121], v[120:121], v[120:121], v[122:123]
	v_mov_b32_e32 v122, v110
	v_mov_b32_e32 v123, v106
	v_pk_mul_f32 v[124:125], v[124:125], v[124:125]
	v_fmamk_f32 v105, v119, 0xba000000, v105
	v_pk_fma_f32 v[122:123], v[122:123], v[122:123], v[124:125]
	v_fmac_f32_e32 v104, 0xba000000, v119
; #define GAS __attribute__((address_space(1)))
; #define LAS __attribute__((address_space(3)))
; __device__ __forceinline__ unsigned cvt_pk_bf16(float lo, float hi) { const f32x2_t_ v = {lo, hi}; const bf16x2_t_ b = __builtin_convertvector(v, bf16x2_t_); return __builtin_bit_cast(unsigned, b); }
; template <bool SKIP_MIX>
; __device__ __forceinline__ void p8_ln_router(Frame& F0, const In& I) {
;     ...
;             const float mean = wave_sum(s) * (1.f / D); float s2 = 0.f;
; #pragma unroll
;             for (int j = 0; j < 8; ++j) { v[j] = v[j] - mean; s2 += (v[j].x * v[j].x + v[j].y * v[j].y) + (v[j].z * v[j].z + v[j].w * v[j].w); }
;             const float rstd = 1.f / sqrtf(wave_sum(s2) * (1.f / D) + LN_EPS);
;             GAS v2u* h1 = (GAS v2u*)((bf16*)(F.ws + WS_H1) + tok * D) + lane;
;             GAS unsigned* h1b = (GAS unsigned*)((unsigned char*)(F.ws + WS_H1B) + tok * D) + lane;
; #pragma unroll
;             for (int j = 0; j < 8; ++j) { f32x4 h;
; #pragma unroll
;                 for (int e = 0; e < 4; ++e) h[e] = v[j][e] * rstd * ln_w[4 * j + e] + ln_b[4 * j + e];
;                 h1[64 * j] = (v2u){pg8::cvt_pk_bf16(h.x, h.y), pg8::cvt_pk_bf16(h.z, h.w)}; { int w8 = __builtin_amdgcn_cvt_pk_fp8_f32(h.x, h.y, 0, false); w8 = __builtin_amdgcn_cvt_pk_fp8_f32(h.z, h.w, w8, true); h1b[64 * j] = (unsigned)w8; }
;                 *(LAS f32x4*)(hs + tl * P8_PITCH + 4 * lane + 256 * j) = h; }
	v_pk_add_f32 v[120:121], v[120:121], v[122:123]
	v_fmamk_f32 v95, v119, 0xba000000, v95
	v_fmac_f32_e32 v94, 0xba000000, v119
	v_pk_add_f32 v[120:121], v[120:121], v[120:121] op_sel_hi:[0,1]
	v_pk_mul_f32 v[122:123], v[94:95], v[94:95]
	v_pk_mul_f32 v[124:125], v[104:105], v[104:105]
	v_fmac_f32_e32 v102, 0xba000000, v119
	v_pk_mov_b32 v[126:127], v[124:125], v[122:123] op_sel:[1,0]
	v_mov_b32_e32 v125, v123
	v_fmac_f32_e32 v92, 0xba000000, v119
	v_fmamk_f32 v103, v119, 0xba000000, v103
	v_mul_f32_e32 v120, v102, v102
	v_pk_add_f32 v[122:123], v[126:127], v[124:125]
	v_fmamk_f32 v93, v119, 0xba000000, v93
	v_pk_fma_f32 v[124:125], v[102:103], v[102:103], v[120:121] op_sel_hi:[1,1,0]
	v_mul_f32_e32 v120, v92, v92
	v_pk_add_f32 v[122:123], v[122:123], v[122:123] op_sel_hi:[0,1]
	v_pk_fma_f32 v[126:127], v[92:93], v[92:93], v[120:121] op_sel_hi:[1,1,0]
	v_fmamk_f32 v73, v119, 0xba000000, v73
	v_fmac_f32_e32 v72, 0xba000000, v119
	v_fmamk_f32 v101, v119, 0xba000000, v101
	v_fmac_f32_e32 v100, 0xba000000, v119
	v_mul_f32_e32 v124, v100, v100
	v_mul_f32_e32 v126, v101, v101
	v_mul_f32_e32 v122, v72, v72
	v_mul_f32_e32 v120, v73, v73
	v_pk_add_f32 v[124:125], v[124:125], v[126:127]
	v_pk_add_f32 v[120:121], v[122:123], v[120:121]
	v_fmamk_f32 v97, v119, 0xba000000, v97
	v_pk_add_f32 v[120:121], v[124:125], v[120:121]
	v_fmac_f32_e32 v96, 0xba000000, v119
	v_fmamk_f32 v91, v119, 0xba000000, v91
	v_fmac_f32_e32 v90, 0xba000000, v119
	v_pk_add_f32 v[120:121], v[120:121], v[120:121] op_sel_hi:[0,1]
	v_pk_mul_f32 v[122:123], v[90:91], v[90:91]
	v_pk_mul_f32 v[124:125], v[96:97], v[96:97]
	v_fmac_f32_e32 v98, 0xba000000, v119
	v_pk_mov_b32 v[126:127], v[124:125], v[122:123] op_sel:[1,0]
	v_mov_b32_e32 v125, v123
	v_fmac_f32_e32 v70, 0xba000000, v119
	v_fmamk_f32 v99, v119, 0xba000000, v99
	v_mul_f32_e32 v120, v98, v98
	v_pk_add_f32 v[122:123], v[126:127], v[124:125]
	v_fmamk_f32 v71, v119, 0xba000000, v71
	v_pk_fma_f32 v[124:125], v[98:99], v[98:99], v[120:121] op_sel_hi:[1,1,0]
	v_mul_f32_e32 v120, v70, v70
	v_pk_add_f32 v[122:123], v[122:123], v[122:123] op_sel_hi:[0,1]
	v_pk_fma_f32 v[126:127], v[70:71], v[70:71], v[120:121] op_sel_hi:[1,1,0]
	v_fmamk_f32 v115, v119, 0xba000000, v115
	v_fmac_f32_e32 v114, 0xba000000, v119
	v_fmamk_f32 v117, v119, 0xba000000, v117
	v_fmac_f32_e32 v116, 0xba000000, v119
	v_mul_f32_e32 v124, v116, v116
	v_mul_f32_e32 v126, v117, v117
	v_mul_f32_e32 v122, v114, v114
	v_mul_f32_e32 v120, v115, v115
	v_pk_add_f32 v[124:125], v[124:125], v[126:127]
	v_pk_add_f32 v[120:121], v[122:123], v[120:121]
	v_mov_b32_e32 v122, 0
	v_pk_add_f32 v[120:121], v[124:125], v[120:121]
	s_nop 0
	v_add_f32_e32 v119, v120, v121
	s_nop 1
	v_add_f32_dpp v119, v119, v119 quad_perm:[1,0,3,2] row_mask:0xf bank_mask:0xf bound_ctrl:1
	s_nop 1
	v_add_f32_dpp v119, v119, v119 quad_perm:[2,3,0,1] row_mask:0xf bank_mask:0xf bound_ctrl:1
	s_nop 1
	v_add_f32_dpp v119, v119, v119 row_ror:4 row_mask:0xf bank_mask:0xf bound_ctrl:1
	s_nop 1
	v_add_f32_dpp v119, v119, v119 row_ror:8 row_mask:0xf bank_mask:0xf bound_ctrl:1
	s_nop 0
	v_readlane_b32 s14, v119, 16
	v_readlane_b32 s15, v119, 48
	v_readlane_b32 s0, v119, 0
	v_readlane_b32 s1, v119, 32
	v_mov_b32_e32 v120, s14
	v_mov_b32_e32 v121, s15
	v_pk_add_f32 v[120:121], s[0:1], v[120:121]
	s_nop 0
	v_add_f32_e32 v119, v120, v121
	v_fmamk_f32 v119, v119, 0x3a000000, v76
	v_mul_f32_e32 v120, 0x4f800000, v119
	v_cmp_gt_f32_e32 vcc, s20, v119
	s_nop 1
	v_cndmask_b32_e32 v120, v119, v120, vcc
	v_sqrt_f32_e32 v121, v120
	v_cvt_pk_bf16_f32 v119, v68, v69
	global_store_dwordx2 v[144:145], v[118:119], off offset:3584
	global_store_dword v[150:151], v128, off offset:1792
	ds_write_b128 v161, v[66:69] offset:7168
	v_add_u32_e32 v118, -1, v121
	v_fma_f32 v119, -v118, v121, v120
	v_cmp_ge_f32_e64 s[0:1], 0, v119
	v_add_u32_e32 v119, 1, v121
	s_nop 0
	v_cndmask_b32_e64 v118, v121, v118, s[0:1]
	v_fma_f32 v121, -v119, v121, v120
	v_cmp_lt_f32_e64 s[0:1], 0, v121
	s_nop 1
	v_cndmask_b32_e64 v118, v118, v119, s[0:1]
	v_mul_f32_e32 v119, 0x37800000, v118
	v_cndmask_b32_e32 v118, v118, v119, vcc
	v_cmp_class_f32_e32 vcc, v120, v155
	s_nop 1
	v_cndmask_b32_e32 v118, v118, v120, vcc
	v_div_scale_f32 v119, s[0:1], v118, v118, 1.0
	v_rcp_f32_e32 v120, v119
	s_add_i32 s0, s23, s13
	s_ashr_i32 s1, s0, 31
	s_lshl_b64 s[14:15], s[0:1], 11
	v_fma_f32 v66, -v119, v120, 1.0
	v_fmac_f32_e32 v120, v66, v120
	v_div_scale_f32 v66, vcc, 1.0, v118, 1.0
	v_mul_f32_e32 v67, v66, v120
	v_fma_f32 v68, -v119, v67, v66
	v_fmac_f32_e32 v67, v68, v120
	v_fma_f32 v66, -v119, v67, v66
	v_div_fmas_f32 v66, v66, v120, v67
	v_div_fixup_f32 v118, v66, v118, 1.0
	v_pk_mul_f32 v[66:67], v[112:113], v[118:119] op_sel_hi:[1,0]
	v_mov_b32_e32 v119, 0
	v_pk_fma_f32 v[66:67], v[2:3], v[66:67], v[6:7]
	s_lshl_b64 s[0:1], s[0:1], 12
	v_cvt_pk_fp8_f32 v119, v66, v67
	v_lshl_add_u64 v[120:121], v[84:85], 0, s[0:1]
	v_lshl_add_u64 v[112:113], v[86:87], 0, s[14:15]
	s_mov_b64 s[0:1], 0
	v_pk_mul_f32 v[68:69], v[110:111], v[118:119] op_sel_hi:[1,0]
	v_cvt_pk_bf16_f32 v110, v66, v67
	v_pk_fma_f32 v[68:69], v[4:5], v[68:69], v[8:9]
	s_nop 0
	v_cvt_pk_fp8_f32 v119, v68, v69 op_sel:[0,0,1]
	v_cvt_pk_bf16_f32 v111, v68, v69
	global_store_dwordx2 v[120:121], v[110:111], off
	global_store_dword v[112:113], v119, off
	v_add_u32_e32 v119, s18, v75
	v_pk_mul_f32 v[108:109], v[108:109], v[118:119] op_sel_hi:[1,0]
	ds_write_b128 v119, v[66:69]
	v_pk_fma_f32 v[108:109], v[10:11], v[108:109], v[14:15]
	v_pk_mul_f32 v[66:67], v[106:107], v[118:119] op_sel_hi:[1,0]
	v_cvt_pk_fp8_f32 v122, v108, v109
	v_pk_fma_f32 v[110:111], v[12:13], v[66:67], v[16:17]
	v_cvt_pk_bf16_f32 v66, v108, v109
; #define LAS __attribute__((address_space(3)))
; __device__ __forceinline__ unsigned cvt_pk_bf16(float lo, float hi) { const f32x2_t_ v = {lo, hi}; const bf16x2_t_ b = __builtin_convertvector(v, bf16x2_t_); return __builtin_bit_cast(unsigned, b); }
; template <bool SKIP_MIX>
; __device__ __forceinline__ void p8_ln_router(Frame& F0, const In& I) {
;     ...
;             for (int j = 0; j < 8; ++j) { f32x4 h;
; #pragma unroll
;                 for (int e = 0; e < 4; ++e) h[e] = v[j][e] * rstd * ln_w[4 * j + e] + ln_b[4 * j + e];
;                 h1[64 * j] = (v2u){pg8::cvt_pk_bf16(h.x, h.y), pg8::cvt_pk_bf16(h.z, h.w)}; { int w8 = __builtin_amdgcn_cvt_pk_fp8_f32(h.x, h.y, 0, false); w8 = __builtin_amdgcn_cvt_pk_fp8_f32(h.z, h.w, w8, true); h1b[64 * j] = (unsigned)w8; }
;                 *(LAS f32x4*)(hs + tl * P8_PITCH + 4 * lane + 256 * j) = h; }
;           } }
;         __syncthreads();
;         f32x4 c0 = (f32x4){0.f, 0.f, 0.f, 0.f}, c1 = c0;
;         const LAS float* ap = hs + col * P8_PITCH + 256 * w + 4 * kq;
;         const float* bp = I.w_router + (size_t)(256 * w + 4 * kq) * NE + col;
; #pragma unroll 4
;         for (int kk = 0; kk < 16; ++kk) {
;             const f32x4 a = *(const LAS f32x4*)(ap + 16 * kk);
; #pragma unroll
;             for (int e = 0; e < 4; ++e) {
;                 const float b0 = bp[(size_t)(16 * kk + e) * NE], b1 = bp[(size_t)(16 * kk + e) * NE + 16];
	v_cvt_pk_bf16_f32 v67, v110, v111
	v_cvt_pk_fp8_f32 v122, v110, v111 op_sel:[0,0,1]
	global_store_dwordx2 v[120:121], v[66:67], off offset:512
	global_store_dword v[112:113], v122, off offset:256
	v_pk_mul_f32 v[66:67], v[104:105], v[118:119] op_sel_hi:[1,0]
	v_mov_b32_e32 v104, 0
	v_pk_fma_f32 v[66:67], v[18:19], v[66:67], v[22:23]
	v_pk_mul_f32 v[68:69], v[94:95], v[118:119] op_sel_hi:[1,0]
	v_cvt_pk_fp8_f32 v104, v66, v67
	v_pk_fma_f32 v[68:69], v[20:21], v[68:69], v[24:25]
	v_cvt_pk_bf16_f32 v94, v66, v67
	v_cvt_pk_bf16_f32 v95, v68, v69
	v_cvt_pk_fp8_f32 v104, v68, v69 op_sel:[0,0,1]
	ds_write_b128 v119, v[108:111] offset:1024
	global_store_dwordx2 v[120:121], v[94:95], off offset:1024
	global_store_dword v[112:113], v104, off offset:512
	v_pk_mul_f32 v[94:95], v[102:103], v[118:119] op_sel_hi:[1,0]
	ds_write_b128 v119, v[66:69] offset:2048
	v_pk_fma_f32 v[102:103], v[26:27], v[94:95], v[30:31]
	v_mov_b32_e32 v94, 0
	v_cvt_pk_fp8_f32 v94, v102, v103
	v_pk_mul_f32 v[66:67], v[92:93], v[118:119] op_sel_hi:[1,0]
	v_mov_b32_e32 v92, 0
	v_pk_fma_f32 v[104:105], v[28:29], v[66:67], v[32:33]
	v_cvt_pk_bf16_f32 v66, v102, v103
	v_cvt_pk_fp8_f32 v94, v104, v105 op_sel:[0,0,1]
	v_cvt_pk_bf16_f32 v67, v104, v105
	global_store_dwordx2 v[120:121], v[66:67], off offset:1536
	global_store_dword v[112:113], v94, off offset:768
	v_pk_mul_f32 v[66:67], v[100:101], v[118:119] op_sel_hi:[1,0]
	v_pk_mul_f32 v[68:69], v[72:73], v[118:119] op_sel_hi:[1,0]
	v_pk_fma_f32 v[66:67], v[34:35], v[66:67], v[42:43]
	v_pk_fma_f32 v[68:69], v[36:37], v[68:69], v[44:45]
	v_cvt_pk_fp8_f32 v92, v66, v67
	v_cvt_pk_bf16_f32 v72, v66, v67
	v_cvt_pk_bf16_f32 v73, v68, v69
	ds_write_b128 v119, v[102:105] offset:3072
	v_cvt_pk_fp8_f32 v92, v68, v69 op_sel:[0,0,1]
	global_store_dwordx2 v[120:121], v[72:73], off offset:2048
	global_store_dword v[112:113], v92, off offset:1024
	v_pk_mul_f32 v[72:73], v[96:97], v[118:119] op_sel_hi:[1,0]
	ds_write_b128 v119, v[66:69] offset:4096
	v_pk_fma_f32 v[92:93], v[38:39], v[72:73], v[46:47]
	v_mov_b32_e32 v72, 0
	v_cvt_pk_fp8_f32 v72, v92, v93
	v_pk_mul_f32 v[66:67], v[90:91], v[118:119] op_sel_hi:[1,0]
	v_pk_mul_f32 v[68:69], v[70:71], v[118:119] op_sel_hi:[1,0]
	v_pk_fma_f32 v[94:95], v[40:41], v[66:67], v[48:49]
	v_cvt_pk_bf16_f32 v66, v92, v93
	v_cvt_pk_fp8_f32 v72, v94, v95 op_sel:[0,0,1]
	v_cvt_pk_bf16_f32 v67, v94, v95
	global_store_dwordx2 v[120:121], v[66:67], off offset:2560
	global_store_dword v[112:113], v72, off offset:1280
	v_pk_mul_f32 v[66:67], v[98:99], v[118:119] op_sel_hi:[1,0]
	v_mov_b32_e32 v72, 0
	v_pk_fma_f32 v[66:67], v[50:51], v[66:67], v[58:59]
	v_pk_fma_f32 v[68:69], v[52:53], v[68:69], v[60:61]
	v_cvt_pk_fp8_f32 v72, v66, v67
	v_cvt_pk_bf16_f32 v70, v66, v67
	v_cvt_pk_bf16_f32 v71, v68, v69
	ds_write_b128 v119, v[92:95] offset:5120
	v_cvt_pk_fp8_f32 v72, v68, v69 op_sel:[0,0,1]
	global_store_dwordx2 v[120:121], v[70:71], off offset:3072
	global_store_dword v[112:113], v72, off offset:1536
	v_pk_mul_f32 v[70:71], v[116:117], v[118:119] op_sel_hi:[1,0]
	v_mov_b32_e32 v90, 0
	v_pk_fma_f32 v[70:71], v[54:55], v[70:71], v[62:63]
	ds_write_b128 v119, v[66:69] offset:6144
	v_cvt_pk_fp8_f32 v90, v70, v71
	v_pk_mul_f32 v[66:67], v[114:115], v[118:119] op_sel_hi:[1,0]
	v_mov_b32_e32 v68, v77
	v_pk_fma_f32 v[72:73], v[56:57], v[66:67], v[64:65]
	v_cvt_pk_bf16_f32 v66, v70, v71
	v_cvt_pk_fp8_f32 v90, v72, v73 op_sel:[0,0,1]
	v_cvt_pk_bf16_f32 v67, v72, v73
	global_store_dwordx2 v[120:121], v[66:67], off offset:3584
	global_store_dword v[112:113], v90, off offset:1792
	ds_write_b128 v119, v[70:73] offset:7168
	v_mov_b32_e32 v90, v152
	v_mov_b32_e32 v66, 0
	v_mov_b32_e32 v67, v77
	v_mov_b32_e32 v69, v77
	v_mov_b32_e32 v70, 0
	v_mov_b32_e32 v71, v77
	v_mov_b32_e32 v72, v77
	v_mov_b32_e32 v73, v77
	s_waitcnt vmcnt(19)
	s_mov_b64 s[0:1], 0x1000
	v_mov_b32_e32 v108, v88
	v_mov_b32_e32 v109, v89
	global_load_dword v117, v[108:109], off offset:0
	global_load_dword v118, v[108:109], off offset:64
	global_load_dword v119, v[108:109], off offset:128
	global_load_dword v120, v[108:109], off offset:192
	global_load_dword v121, v[108:109], off offset:256
	global_load_dword v122, v[108:109], off offset:320
	global_load_dword v123, v[108:109], off offset:384
	global_load_dword v124, v[108:109], off offset:448
	global_load_dword v125, v[108:109], off offset:2048
	global_load_dword v126, v[108:109], off offset:2112
	global_load_dword v127, v[108:109], off offset:2176
	global_load_dword v128, v[108:109], off offset:2240
	global_load_dword v129, v[108:109], off offset:2304
	global_load_dword v130, v[108:109], off offset:2368
	global_load_dword v131, v[108:109], off offset:2432
	global_load_dword v132, v[108:109], off offset:2496
	v_lshl_add_u64 v[108:109], v[108:109], 0, s[0:1]
	global_load_dword v133, v[108:109], off offset:0
	global_load_dword v134, v[108:109], off offset:64
	global_load_dword v135, v[108:109], off offset:128
	global_load_dword v136, v[108:109], off offset:192
	global_load_dword v137, v[108:109], off offset:256
	global_load_dword v138, v[108:109], off offset:320
	global_load_dword v139, v[108:109], off offset:384
	global_load_dword v140, v[108:109], off offset:448
	global_load_dword v141, v[108:109], off offset:2048
	global_load_dword v142, v[108:109], off offset:2112
	global_load_dword v143, v[108:109], off offset:2176
	global_load_dword v144, v[108:109], off offset:2240
	global_load_dword v145, v[108:109], off offset:2304
	global_load_dword v146, v[108:109], off offset:2368
	global_load_dword v147, v[108:109], off offset:2432
	global_load_dword v148, v[108:109], off offset:2496
	v_lshl_add_u64 v[108:109], v[108:109], 0, s[0:1]
	global_load_dword v149, v[108:109], off offset:0
	global_load_dword v150, v[108:109], off offset:64
	global_load_dword v151, v[108:109], off offset:128
	global_load_dword v160, v[108:109], off offset:192
	global_load_dword v161, v[108:109], off offset:256
	global_load_dword v162, v[108:109], off offset:320
	global_load_dword v163, v[108:109], off offset:384
	global_load_dword v164, v[108:109], off offset:448
	global_load_dword v165, v[108:109], off offset:2048
	global_load_dword v166, v[108:109], off offset:2112
	global_load_dword v167, v[108:109], off offset:2176
	global_load_dword v168, v[108:109], off offset:2240
	s_waitcnt lgkmcnt(0)
	s_barrier
; #define LAS __attribute__((address_space(3)))
; template <bool SKIP_MIX>
; __device__ __forceinline__ void p8_ln_router(Frame& F0, const In& I) {
;     ...
;         for (int kk = 0; kk < 16; ++kk) {
;             const f32x4 a = *(const LAS f32x4*)(ap + 16 * kk);
; #pragma unroll
;             for (int e = 0; e < 4; ++e) {
;                 const float b0 = bp[(size_t)(16 * kk + e) * NE], b1 = bp[(size_t)(16 * kk + e) * NE + 16];
;                 c0 = __builtin_amdgcn_mfma_f32_16x16x4f32(a[e], b0, c0, 0, 0, 0);
;                 c1 = __builtin_amdgcn_mfma_f32_16x16x4f32(a[e], b1, c1, 0, 0, 0);
;             }
;         }
.LBB0_1515:
	ds_read_b128 v[92:95], v90
	ds_read_b128 v[96:99], v90 offset:64
	ds_read_b128 v[100:103], v90 offset:128
	ds_read_b128 v[104:107], v90 offset:192
	s_waitcnt lgkmcnt(3)
	global_load_dword v169, v[108:109], off offset:2304
	s_waitcnt vmcnt(43)
	v_mfma_f32_16x16x4_f32 v[66:69], v92, v117, v[66:69]
	v_mfma_f32_16x16x4_f32 v[70:73], v92, v118, v[70:73]
	global_load_dword v170, v[108:109], off offset:2368
	s_waitcnt vmcnt(42)
	v_mfma_f32_16x16x4_f32 v[66:69], v93, v119, v[66:69]
	v_mfma_f32_16x16x4_f32 v[70:73], v93, v120, v[70:73]
	global_load_dword v171, v[108:109], off offset:2432
	s_waitcnt vmcnt(41)
	v_mfma_f32_16x16x4_f32 v[66:69], v94, v121, v[66:69]
	v_mfma_f32_16x16x4_f32 v[70:73], v94, v122, v[70:73]
	global_load_dword v172, v[108:109], off offset:2496
	s_waitcnt vmcnt(40)
	v_mfma_f32_16x16x4_f32 v[66:69], v95, v123, v[66:69]
	v_mfma_f32_16x16x4_f32 v[70:73], v95, v124, v[70:73]
	s_waitcnt lgkmcnt(2)
	v_lshl_add_u64 v[108:109], v[108:109], 0, s[0:1]
	global_load_dword v173, v[108:109], off offset:0
	s_waitcnt vmcnt(39)
	v_mfma_f32_16x16x4_f32 v[66:69], v96, v125, v[66:69]
	v_mfma_f32_16x16x4_f32 v[70:73], v96, v126, v[70:73]
	global_load_dword v174, v[108:109], off offset:64
	s_waitcnt vmcnt(38)
	v_mfma_f32_16x16x4_f32 v[66:69], v97, v127, v[66:69]
	v_mfma_f32_16x16x4_f32 v[70:73], v97, v128, v[70:73]
	global_load_dword v175, v[108:109], off offset:128
	s_waitcnt vmcnt(37)
	v_mfma_f32_16x16x4_f32 v[66:69], v98, v129, v[66:69]
	v_mfma_f32_16x16x4_f32 v[70:73], v98, v130, v[70:73]
	global_load_dword v176, v[108:109], off offset:192
	s_waitcnt vmcnt(36)
	v_mfma_f32_16x16x4_f32 v[66:69], v99, v131, v[66:69]
	v_mfma_f32_16x16x4_f32 v[70:73], v99, v132, v[70:73]
	s_waitcnt lgkmcnt(1)
	global_load_dword v177, v[108:109], off offset:256
	s_waitcnt vmcnt(35)
	v_mfma_f32_16x16x4_f32 v[66:69], v100, v133, v[66:69]
	v_mfma_f32_16x16x4_f32 v[70:73], v100, v134, v[70:73]
	global_load_dword v178, v[108:109], off offset:320
	s_waitcnt vmcnt(34)
	v_mfma_f32_16x16x4_f32 v[66:69], v101, v135, v[66:69]
	v_mfma_f32_16x16x4_f32 v[70:73], v101, v136, v[70:73]
	global_load_dword v179, v[108:109], off offset:384
	s_waitcnt vmcnt(33)
	v_mfma_f32_16x16x4_f32 v[66:69], v102, v137, v[66:69]
	v_mfma_f32_16x16x4_f32 v[70:73], v102, v138, v[70:73]
	global_load_dword v180, v[108:109], off offset:448
	s_waitcnt vmcnt(32)
	v_mfma_f32_16x16x4_f32 v[66:69], v103, v139, v[66:69]
	v_mfma_f32_16x16x4_f32 v[70:73], v103, v140, v[70:73]
	s_waitcnt lgkmcnt(0)
	global_load_dword v181, v[108:109], off offset:2048
	s_waitcnt vmcnt(31)
	v_mfma_f32_16x16x4_f32 v[66:69], v104, v141, v[66:69]
	v_mfma_f32_16x16x4_f32 v[70:73], v104, v142, v[70:73]
	global_load_dword v182, v[108:109], off offset:2112
	s_waitcnt vmcnt(30)
	v_mfma_f32_16x16x4_f32 v[66:69], v105, v143, v[66:69]
	v_mfma_f32_16x16x4_f32 v[70:73], v105, v144, v[70:73]
	global_load_dword v183, v[108:109], off offset:2176
	s_waitcnt vmcnt(29)
	v_mfma_f32_16x16x4_f32 v[66:69], v106, v145, v[66:69]
	v_mfma_f32_16x16x4_f32 v[70:73], v106, v146, v[70:73]
	global_load_dword v184, v[108:109], off offset:2240
	s_waitcnt vmcnt(28)
	v_mfma_f32_16x16x4_f32 v[66:69], v107, v147, v[66:69]
	v_mfma_f32_16x16x4_f32 v[70:73], v107, v148, v[70:73]
	ds_read_b128 v[92:95], v90 offset:256
	ds_read_b128 v[96:99], v90 offset:320
	ds_read_b128 v[100:103], v90 offset:384
	ds_read_b128 v[104:107], v90 offset:448
	s_waitcnt lgkmcnt(3)
	global_load_dword v185, v[108:109], off offset:2304
	s_waitcnt vmcnt(27)
	v_mfma_f32_16x16x4_f32 v[66:69], v92, v149, v[66:69]
	v_mfma_f32_16x16x4_f32 v[70:73], v92, v150, v[70:73]
	global_load_dword v186, v[108:109], off offset:2368
	s_waitcnt vmcnt(26)
	v_mfma_f32_16x16x4_f32 v[66:69], v93, v151, v[66:69]
	v_mfma_f32_16x16x4_f32 v[70:73], v93, v160, v[70:73]
	global_load_dword v187, v[108:109], off offset:2432
	s_waitcnt vmcnt(25)
	v_mfma_f32_16x16x4_f32 v[66:69], v94, v161, v[66:69]
	v_mfma_f32_16x16x4_f32 v[70:73], v94, v162, v[70:73]
	global_load_dword v188, v[108:109], off offset:2496
	s_waitcnt vmcnt(24)
	v_mfma_f32_16x16x4_f32 v[66:69], v95, v163, v[66:69]
	v_mfma_f32_16x16x4_f32 v[70:73], v95, v164, v[70:73]
	s_waitcnt lgkmcnt(2)
	v_lshl_add_u64 v[108:109], v[108:109], 0, s[0:1]
	global_load_dword v189, v[108:109], off offset:0
	s_waitcnt vmcnt(23)
	v_mfma_f32_16x16x4_f32 v[66:69], v96, v165, v[66:69]
	v_mfma_f32_16x16x4_f32 v[70:73], v96, v166, v[70:73]
	global_load_dword v190, v[108:109], off offset:64
	s_waitcnt vmcnt(22)
	v_mfma_f32_16x16x4_f32 v[66:69], v97, v167, v[66:69]
	v_mfma_f32_16x16x4_f32 v[70:73], v97, v168, v[70:73]
	global_load_dword v191, v[108:109], off offset:128
	s_waitcnt vmcnt(21)
	v_mfma_f32_16x16x4_f32 v[66:69], v98, v169, v[66:69]
	v_mfma_f32_16x16x4_f32 v[70:73], v98, v170, v[70:73]
	global_load_dword v192, v[108:109], off offset:192
	s_waitcnt vmcnt(20)
	v_mfma_f32_16x16x4_f32 v[66:69], v99, v171, v[66:69]
	v_mfma_f32_16x16x4_f32 v[70:73], v99, v172, v[70:73]
	s_waitcnt lgkmcnt(1)
	global_load_dword v193, v[108:109], off offset:256
	s_waitcnt vmcnt(19)
	v_mfma_f32_16x16x4_f32 v[66:69], v100, v173, v[66:69]
	v_mfma_f32_16x16x4_f32 v[70:73], v100, v174, v[70:73]
	global_load_dword v194, v[108:109], off offset:320
	s_waitcnt vmcnt(18)
	v_mfma_f32_16x16x4_f32 v[66:69], v101, v175, v[66:69]
	v_mfma_f32_16x16x4_f32 v[70:73], v101, v176, v[70:73]
	global_load_dword v195, v[108:109], off offset:384
	s_waitcnt vmcnt(17)
	v_mfma_f32_16x16x4_f32 v[66:69], v102, v177, v[66:69]
	v_mfma_f32_16x16x4_f32 v[70:73], v102, v178, v[70:73]
	global_load_dword v196, v[108:109], off offset:448
	s_waitcnt vmcnt(16)
	v_mfma_f32_16x16x4_f32 v[66:69], v103, v179, v[66:69]
	v_mfma_f32_16x16x4_f32 v[70:73], v103, v180, v[70:73]
	s_waitcnt lgkmcnt(0)
; #define LAS __attribute__((address_space(3)))
; template <bool SKIP_MIX>
; __device__ __forceinline__ void p8_ln_router(Frame& F0, const In& I) {
;     ...
;         for (int kk = 0; kk < 16; ++kk) {
;             const f32x4 a = *(const LAS f32x4*)(ap + 16 * kk);
; #pragma unroll
;             for (int e = 0; e < 4; ++e) {
;                 const float b0 = bp[(size_t)(16 * kk + e) * NE], b1 = bp[(size_t)(16 * kk + e) * NE + 16];
;                 c0 = __builtin_amdgcn_mfma_f32_16x16x4f32(a[e], b0, c0, 0, 0, 0);
;                 c1 = __builtin_amdgcn_mfma_f32_16x16x4f32(a[e], b1, c1, 0, 0, 0);
;             }
;         }
; #pragma unroll
;         for (int i = 0; i < 4; ++i) { part[(w * 16 + 4 * kq + i) * 32 + col] = c0[i]; part[(w * 16 + 4 * kq + i) * 32 + 16 + col] = c1[i]; }
;         __syncthreads();
;         { const int tl = F.tid >> 5, e = F.tid & 31; float s = I.b_router[e];
; #pragma unroll
;             for (int ww = 0; ww < 8; ++ww) s += part[(ww * 16 + tl) * 32 + e];
;             lg[tl * 32 + e] = s; }
;         __syncthreads();
	global_load_dword v197, v[108:109], off offset:2048
	s_waitcnt vmcnt(15)
	v_mfma_f32_16x16x4_f32 v[66:69], v104, v181, v[66:69]
	v_mfma_f32_16x16x4_f32 v[70:73], v104, v182, v[70:73]
	global_load_dword v198, v[108:109], off offset:2112
	s_waitcnt vmcnt(14)
	v_mfma_f32_16x16x4_f32 v[66:69], v105, v183, v[66:69]
	v_mfma_f32_16x16x4_f32 v[70:73], v105, v184, v[70:73]
	global_load_dword v199, v[108:109], off offset:2176
	s_waitcnt vmcnt(13)
	v_mfma_f32_16x16x4_f32 v[66:69], v106, v185, v[66:69]
	v_mfma_f32_16x16x4_f32 v[70:73], v106, v186, v[70:73]
	s_waitcnt vmcnt(11)
	v_mfma_f32_16x16x4_f32 v[66:69], v107, v187, v[66:69]
	v_mfma_f32_16x16x4_f32 v[70:73], v107, v188, v[70:73]
	ds_read_b128 v[92:95], v90 offset:512
	ds_read_b128 v[96:99], v90 offset:576
	ds_read_b128 v[100:103], v90 offset:640
	ds_read_b128 v[104:107], v90 offset:704
	s_waitcnt lgkmcnt(3)
	s_waitcnt vmcnt(9)
	v_mfma_f32_16x16x4_f32 v[66:69], v92, v189, v[66:69]
	v_mfma_f32_16x16x4_f32 v[70:73], v92, v190, v[70:73]
	s_waitcnt vmcnt(7)
	v_mfma_f32_16x16x4_f32 v[66:69], v93, v191, v[66:69]
	v_mfma_f32_16x16x4_f32 v[70:73], v93, v192, v[70:73]
	s_waitcnt vmcnt(5)
	v_mfma_f32_16x16x4_f32 v[66:69], v94, v193, v[66:69]
	v_mfma_f32_16x16x4_f32 v[70:73], v94, v194, v[70:73]
	s_waitcnt vmcnt(3)
	v_mfma_f32_16x16x4_f32 v[66:69], v95, v195, v[66:69]
	v_mfma_f32_16x16x4_f32 v[70:73], v95, v196, v[70:73]
	s_waitcnt lgkmcnt(2)
	s_waitcnt vmcnt(1)
	v_mfma_f32_16x16x4_f32 v[66:69], v96, v197, v[66:69]
	v_mfma_f32_16x16x4_f32 v[70:73], v96, v198, v[70:73]
	s_waitcnt vmcnt(0)
	v_mfma_f32_16x16x4_f32 v[66:69], v97, v199, v[66:69]
	v_mfma_f32_16x16x4_f32 v[70:73], v97, v200, v[70:73]
	v_mfma_f32_16x16x4_f32 v[66:69], v98, v201, v[66:69]
	v_mfma_f32_16x16x4_f32 v[70:73], v98, v202, v[70:73]
	v_mfma_f32_16x16x4_f32 v[66:69], v99, v203, v[66:69]
	v_mfma_f32_16x16x4_f32 v[70:73], v99, v204, v[70:73]
	s_waitcnt lgkmcnt(1)
	v_mfma_f32_16x16x4_f32 v[66:69], v100, v205, v[66:69]
	v_mfma_f32_16x16x4_f32 v[70:73], v100, v206, v[70:73]
	v_mfma_f32_16x16x4_f32 v[66:69], v101, v207, v[66:69]
	v_mfma_f32_16x16x4_f32 v[70:73], v101, v208, v[70:73]
	v_mfma_f32_16x16x4_f32 v[66:69], v102, v209, v[66:69]
	v_mfma_f32_16x16x4_f32 v[70:73], v102, v210, v[70:73]
	v_mfma_f32_16x16x4_f32 v[66:69], v103, v211, v[66:69]
	v_mfma_f32_16x16x4_f32 v[70:73], v103, v212, v[70:73]
	s_waitcnt lgkmcnt(0)
	v_mfma_f32_16x16x4_f32 v[66:69], v104, v213, v[66:69]
	v_mfma_f32_16x16x4_f32 v[70:73], v104, v214, v[70:73]
	v_mfma_f32_16x16x4_f32 v[66:69], v105, v215, v[66:69]
	v_mfma_f32_16x16x4_f32 v[70:73], v105, v216, v[70:73]
	v_mfma_f32_16x16x4_f32 v[66:69], v106, v217, v[66:69]
	v_mfma_f32_16x16x4_f32 v[70:73], v106, v218, v[70:73]
	v_mfma_f32_16x16x4_f32 v[66:69], v107, v219, v[66:69]
	v_mfma_f32_16x16x4_f32 v[70:73], v107, v220, v[70:73]
	ds_read_b128 v[92:95], v90 offset:768
	ds_read_b128 v[96:99], v90 offset:832
	ds_read_b128 v[100:103], v90 offset:896
	ds_read_b128 v[104:107], v90 offset:960
	s_waitcnt lgkmcnt(3)
	v_mfma_f32_16x16x4_f32 v[66:69], v92, v221, v[66:69]
	v_mfma_f32_16x16x4_f32 v[70:73], v92, v222, v[70:73]
	v_mfma_f32_16x16x4_f32 v[66:69], v93, v223, v[66:69]
	v_mfma_f32_16x16x4_f32 v[70:73], v93, v224, v[70:73]
	v_mfma_f32_16x16x4_f32 v[66:69], v94, v225, v[66:69]
	v_mfma_f32_16x16x4_f32 v[70:73], v94, v226, v[70:73]
	v_mfma_f32_16x16x4_f32 v[66:69], v95, v227, v[66:69]
	v_mfma_f32_16x16x4_f32 v[70:73], v95, v228, v[70:73]
	s_waitcnt lgkmcnt(2)
	v_mfma_f32_16x16x4_f32 v[66:69], v96, v229, v[66:69]
	v_mfma_f32_16x16x4_f32 v[70:73], v96, v230, v[70:73]
	v_mfma_f32_16x16x4_f32 v[66:69], v97, v231, v[66:69]
	v_mfma_f32_16x16x4_f32 v[70:73], v97, v232, v[70:73]
	v_mfma_f32_16x16x4_f32 v[66:69], v98, v233, v[66:69]
	v_mfma_f32_16x16x4_f32 v[70:73], v98, v234, v[70:73]
	v_mfma_f32_16x16x4_f32 v[66:69], v99, v235, v[66:69]
	v_mfma_f32_16x16x4_f32 v[70:73], v99, v236, v[70:73]
	s_waitcnt lgkmcnt(1)
	v_mfma_f32_16x16x4_f32 v[66:69], v100, v237, v[66:69]
	v_mfma_f32_16x16x4_f32 v[70:73], v100, v238, v[70:73]
	v_mfma_f32_16x16x4_f32 v[66:69], v101, v239, v[66:69]
	v_mfma_f32_16x16x4_f32 v[70:73], v101, v240, v[70:73]
	v_mfma_f32_16x16x4_f32 v[66:69], v102, v241, v[66:69]
	v_mfma_f32_16x16x4_f32 v[70:73], v102, v242, v[70:73]
	v_mfma_f32_16x16x4_f32 v[66:69], v103, v243, v[66:69]
	v_mfma_f32_16x16x4_f32 v[70:73], v103, v244, v[70:73]
	s_waitcnt lgkmcnt(0)
	v_mfma_f32_16x16x4_f32 v[66:69], v104, v245, v[66:69]
	v_mfma_f32_16x16x4_f32 v[70:73], v104, v246, v[70:73]
	v_mfma_f32_16x16x4_f32 v[66:69], v105, v247, v[66:69]
	v_mfma_f32_16x16x4_f32 v[70:73], v105, v248, v[70:73]
	v_mfma_f32_16x16x4_f32 v[66:69], v106, v249, v[66:69]
	v_mfma_f32_16x16x4_f32 v[70:73], v106, v250, v[70:73]
	v_mfma_f32_16x16x4_f32 v[66:69], v107, v251, v[66:69]
	v_mfma_f32_16x16x4_f32 v[70:73], v107, v252, v[70:73]
	s_nop 8
	ds_write2_b32 v156, v66, v70 offset1:16
	ds_write2_b32 v156, v67, v71 offset0:32 offset1:48
	ds_write2_b32 v156, v68, v72 offset0:64 offset1:80
	ds_write2_b32 v156, v69, v73 offset0:96 offset1:112
	s_waitcnt lgkmcnt(0)
	s_barrier
	ds_read2st64_b32 v[66:67], v153 offset1:8
	ds_read2st64_b32 v[68:69], v153 offset0:16 offset1:24
	ds_read2st64_b32 v[70:71], v153 offset0:32 offset1:40
	ds_read2st64_b32 v[72:73], v153 offset0:48 offset1:56
	s_waitcnt lgkmcnt(3)
	v_add_f32_e32 v66, v253, v66
	v_add_f32_e32 v66, v66, v67
	s_waitcnt lgkmcnt(2)
	v_add_f32_e32 v66, v66, v68
	v_add_f32_e32 v66, v66, v69
	s_waitcnt lgkmcnt(1)
	v_add_f32_e32 v66, v66, v70
	v_add_f32_e32 v66, v66, v71
	s_waitcnt lgkmcnt(0)
	v_add_f32_e32 v66, v66, v72
	v_add_f32_e32 v66, v66, v73
	ds_write_b32 v154, v66
	s_waitcnt lgkmcnt(0)
	s_barrier
; template <bool SKIP_MIX>
; __device__ __forceinline__ void p8_ln_router(Frame& F0, const In& I) {
;     ...
;         if (F.tid < 16) {
;             const int tl = F.tid; float lv[32];
; #pragma unroll
;             for (int e = 0; e < 32; ++e) lv[e] = lg[tl * 32 + e];
;             int ti[4]; float tv[4];
; #pragma unroll
;             for (int k = 0; k < 4; ++k) { float best = -3.4e38f; int bi = 0;
; #pragma unroll
;                 for (int e = 0; e < 32; ++e) { const bool tk = lv[e] > best; best = tk ? lv[e] : best; bi = tk ? e : bi; }
;                 ti[k] = bi; tv[k] = best;
; #pragma unroll
;                 for (int e = 0; e < 32; ++e) lv[e] = (e == bi) ? -3.4e38f : lv[e]; }
	s_and_saveexec_b64 s[0:1], s[4:5]
	s_cbranch_execz .LBB0_1513
	ds_read_b128 v[68:71], v157
	ds_read_b128 v[90:93], v157 offset:16
	ds_read_b128 v[94:97], v157 offset:32
	ds_read_b128 v[98:101], v157 offset:48
	ds_read_b128 v[102:105], v157 offset:64
	ds_read_b128 v[106:109], v157 offset:80
	ds_read_b128 v[110:113], v157 offset:96
	ds_read_b128 v[114:117], v157 offset:112
	s_waitcnt lgkmcnt(7)
	v_max_f32_e32 v66, v68, v68
	v_max_f32_e32 v66, 0xff7fc99e, v66
	v_cmp_gt_f32_e32 vcc, v69, v66
	s_nop 1
	v_cndmask_b32_e32 v66, v66, v69, vcc
	v_cndmask_b32_e64 v67, 0, 1, vcc
	v_cmp_gt_f32_e32 vcc, v70, v66
	s_nop 1
	v_cndmask_b32_e32 v66, v66, v70, vcc
	v_cndmask_b32_e64 v67, v67, 2, vcc
	v_cmp_gt_f32_e32 vcc, v71, v66
	s_nop 1
	v_cndmask_b32_e32 v66, v66, v71, vcc
	v_cndmask_b32_e64 v67, v67, 3, vcc
	s_waitcnt lgkmcnt(6)
	v_cmp_gt_f32_e32 vcc, v90, v66
	s_nop 1
	v_cndmask_b32_e32 v66, v66, v90, vcc
	v_cndmask_b32_e64 v67, v67, 4, vcc
	v_cmp_gt_f32_e32 vcc, v91, v66
	s_nop 1
	v_cndmask_b32_e32 v66, v66, v91, vcc
	v_cndmask_b32_e64 v67, v67, 5, vcc
	v_cmp_gt_f32_e32 vcc, v92, v66
	s_nop 1
	v_cndmask_b32_e32 v66, v66, v92, vcc
	v_cndmask_b32_e64 v67, v67, 6, vcc
	v_cmp_gt_f32_e32 vcc, v93, v66
	s_nop 1
	v_cndmask_b32_e32 v66, v66, v93, vcc
	v_cndmask_b32_e64 v67, v67, 7, vcc
	s_waitcnt lgkmcnt(5)
	v_cmp_gt_f32_e32 vcc, v94, v66
	s_nop 1
	v_cndmask_b32_e32 v66, v66, v94, vcc
	v_cndmask_b32_e64 v67, v67, 8, vcc
	v_cmp_gt_f32_e32 vcc, v95, v66
	s_nop 1
	v_cndmask_b32_e32 v66, v66, v95, vcc
	v_cndmask_b32_e64 v67, v67, 9, vcc
	v_cmp_gt_f32_e32 vcc, v96, v66
	s_nop 1
	v_cndmask_b32_e32 v66, v66, v96, vcc
	v_cndmask_b32_e64 v67, v67, 10, vcc
	v_cmp_gt_f32_e32 vcc, v97, v66
	s_nop 1
	v_cndmask_b32_e32 v66, v66, v97, vcc
	v_cndmask_b32_e64 v67, v67, 11, vcc
	s_waitcnt lgkmcnt(4)
	v_cmp_gt_f32_e32 vcc, v98, v66
	s_nop 1
	v_cndmask_b32_e32 v66, v66, v98, vcc
	v_cndmask_b32_e64 v67, v67, 12, vcc
	v_cmp_gt_f32_e32 vcc, v99, v66
	s_nop 1
	v_cndmask_b32_e32 v66, v66, v99, vcc
	v_cndmask_b32_e64 v67, v67, 13, vcc
	v_cmp_gt_f32_e32 vcc, v100, v66
	s_nop 1
	v_cndmask_b32_e32 v66, v66, v100, vcc
	v_cndmask_b32_e64 v67, v67, 14, vcc
	v_cmp_gt_f32_e32 vcc, v101, v66
	s_nop 1
	v_cndmask_b32_e32 v66, v66, v101, vcc
	v_cndmask_b32_e64 v67, v67, 15, vcc
	s_waitcnt lgkmcnt(3)
	v_cmp_gt_f32_e32 vcc, v102, v66
	s_nop 1
	v_cndmask_b32_e32 v66, v66, v102, vcc
	v_cndmask_b32_e64 v67, v67, 16, vcc
	v_cmp_gt_f32_e32 vcc, v103, v66
	s_nop 1
	v_cndmask_b32_e32 v66, v66, v103, vcc
	v_cndmask_b32_e64 v67, v67, 17, vcc
	v_cmp_gt_f32_e32 vcc, v104, v66
	s_nop 1
	v_cndmask_b32_e32 v66, v66, v104, vcc
	v_cndmask_b32_e64 v67, v67, 18, vcc
	v_cmp_gt_f32_e32 vcc, v105, v66
	s_nop 1
	v_cndmask_b32_e32 v66, v66, v105, vcc
	v_cndmask_b32_e64 v67, v67, 19, vcc
	s_waitcnt lgkmcnt(2)
	v_cmp_gt_f32_e32 vcc, v106, v66
	s_nop 1
	v_cndmask_b32_e32 v66, v66, v106, vcc
	v_cndmask_b32_e64 v67, v67, 20, vcc
	v_cmp_gt_f32_e32 vcc, v107, v66
	s_nop 1
	v_cndmask_b32_e32 v66, v66, v107, vcc
	v_cndmask_b32_e64 v67, v67, 21, vcc
	v_cmp_gt_f32_e32 vcc, v108, v66
	s_nop 1
	v_cndmask_b32_e32 v66, v66, v108, vcc
	v_cndmask_b32_e64 v67, v67, 22, vcc
	v_cmp_gt_f32_e32 vcc, v109, v66
	s_nop 1
	v_cndmask_b32_e32 v66, v66, v109, vcc
	v_cndmask_b32_e64 v67, v67, 23, vcc
	s_waitcnt lgkmcnt(1)
	v_cmp_gt_f32_e32 vcc, v110, v66
	s_nop 1
	v_cndmask_b32_e32 v66, v66, v110, vcc
	v_cndmask_b32_e64 v67, v67, 24, vcc
	v_cmp_gt_f32_e32 vcc, v111, v66
	s_nop 1
	v_cndmask_b32_e32 v66, v66, v111, vcc
	v_cndmask_b32_e64 v67, v67, 25, vcc
	v_cmp_gt_f32_e32 vcc, v112, v66
	s_nop 1
	v_cndmask_b32_e32 v66, v66, v112, vcc
	v_cndmask_b32_e64 v67, v67, 26, vcc
	v_cmp_gt_f32_e32 vcc, v113, v66
	s_nop 1
	v_cndmask_b32_e32 v66, v66, v113, vcc
	v_cndmask_b32_e64 v67, v67, 27, vcc
	s_waitcnt lgkmcnt(0)
	v_cmp_gt_f32_e32 vcc, v114, v66
	s_nop 1
	v_cndmask_b32_e32 v66, v66, v114, vcc
	v_cndmask_b32_e64 v67, v67, 28, vcc
	v_cmp_gt_f32_e32 vcc, v115, v66
	s_nop 1
	v_cndmask_b32_e32 v66, v66, v115, vcc
	v_cndmask_b32_e64 v67, v67, 29, vcc
	v_cmp_gt_f32_e32 vcc, v116, v66
	s_nop 1
	v_cndmask_b32_e32 v72, v66, v116, vcc
	v_cndmask_b32_e64 v67, v67, 30, vcc
	v_cmp_gt_f32_e32 vcc, v117, v72
	s_nop 1
	v_cndmask_b32_e64 v66, v67, 31, vcc
	v_cndmask_b32_e32 v73, v72, v117, vcc
	v_cmp_ne_u32_e32 vcc, 0, v66
	s_nop 1
	v_cndmask_b32_e32 v68, v159, v68, vcc
	v_cmp_ne_u32_e32 vcc, 1, v66
	v_max_f32_e32 v67, v68, v68
	v_max_f32_e32 v67, 0xff7fc99e, v67
	v_cndmask_b32_e32 v69, v159, v69, vcc
	v_cmp_ne_u32_e32 vcc, 2, v66
	s_nop 1
	v_cndmask_b32_e32 v70, v159, v70, vcc
	v_cmp_ne_u32_e32 vcc, 3, v66
	s_nop 1
	v_cndmask_b32_e32 v71, v159, v71, vcc
	v_cmp_ne_u32_e32 vcc, 4, v66
	s_nop 1
	v_cndmask_b32_e32 v72, v159, v90, vcc
	v_cmp_ne_u32_e32 vcc, 5, v66
	s_nop 1
	v_cndmask_b32_e32 v90, v159, v91, vcc
	v_cmp_ne_u32_e32 vcc, 6, v66
	s_nop 1
	v_cndmask_b32_e32 v91, v159, v92, vcc
	v_cmp_ne_u32_e32 vcc, 7, v66
	s_nop 1
	v_cndmask_b32_e32 v92, v159, v93, vcc
	v_cmp_ne_u32_e32 vcc, 8, v66
	s_nop 1
	v_cndmask_b32_e32 v93, v159, v94, vcc
	v_cmp_ne_u32_e32 vcc, 9, v66
	s_nop 1
	v_cndmask_b32_e32 v94, v159, v95, vcc
	v_cmp_ne_u32_e32 vcc, 10, v66
	s_nop 1
	v_cndmask_b32_e32 v95, v159, v96, vcc
	v_cmp_ne_u32_e32 vcc, 11, v66
	s_nop 1
	v_cndmask_b32_e32 v96, v159, v97, vcc
	v_cmp_ne_u32_e32 vcc, 12, v66
	s_nop 1
	v_cndmask_b32_e32 v97, v159, v98, vcc
	v_cmp_ne_u32_e32 vcc, 13, v66
	s_nop 1
	v_cndmask_b32_e32 v98, v159, v99, vcc
	v_cmp_ne_u32_e32 vcc, 14, v66
	s_nop 1
	v_cndmask_b32_e32 v99, v159, v100, vcc
	v_cmp_ne_u32_e32 vcc, 15, v66
	s_nop 1
	v_cndmask_b32_e32 v100, v159, v101, vcc
	v_cmp_ne_u32_e32 vcc, 16, v66
	s_nop 1
	v_cndmask_b32_e32 v101, v159, v102, vcc
; template <bool SKIP_MIX>
; __device__ __forceinline__ void p8_ln_router(Frame& F0, const In& I) {
;     ...
;             for (int k = 0; k < 4; ++k) { float best = -3.4e38f; int bi = 0;
; #pragma unroll
;                 for (int e = 0; e < 32; ++e) { const bool tk = lv[e] > best; best = tk ? lv[e] : best; bi = tk ? e : bi; }
;                 ti[k] = bi; tv[k] = best;
; #pragma unroll
;                 for (int e = 0; e < 32; ++e) lv[e] = (e == bi) ? -3.4e38f : lv[e]; }
	v_cmp_ne_u32_e32 vcc, 17, v66
	s_nop 1
	v_cndmask_b32_e32 v102, v159, v103, vcc
	v_cmp_ne_u32_e32 vcc, 18, v66
	s_nop 1
	v_cndmask_b32_e32 v103, v159, v104, vcc
	v_cmp_ne_u32_e32 vcc, 19, v66
	s_nop 1
	v_cndmask_b32_e32 v104, v159, v105, vcc
	v_cmp_ne_u32_e32 vcc, 20, v66
	s_nop 1
	v_cndmask_b32_e32 v105, v159, v106, vcc
	v_cmp_ne_u32_e32 vcc, 21, v66
	s_nop 1
	v_cndmask_b32_e32 v106, v159, v107, vcc
	v_cmp_ne_u32_e32 vcc, 22, v66
	s_nop 1
	v_cndmask_b32_e32 v107, v159, v108, vcc
	v_cmp_ne_u32_e32 vcc, 23, v66
	s_nop 1
	v_cndmask_b32_e32 v108, v159, v109, vcc
	v_cmp_ne_u32_e32 vcc, 24, v66
	s_nop 1
	v_cndmask_b32_e32 v109, v159, v110, vcc
	v_cmp_ne_u32_e32 vcc, 25, v66
	s_nop 1
	v_cndmask_b32_e32 v110, v159, v111, vcc
	v_cmp_ne_u32_e32 vcc, 26, v66
	s_nop 1
	v_cndmask_b32_e32 v111, v159, v112, vcc
	v_cmp_ne_u32_e32 vcc, 27, v66
	s_nop 1
	v_cndmask_b32_e32 v112, v159, v113, vcc
	v_cmp_ne_u32_e32 vcc, 28, v66
	s_nop 1
	v_cndmask_b32_e32 v113, v159, v114, vcc
	v_cmp_ne_u32_e32 vcc, 29, v66
	s_nop 1
	v_cndmask_b32_e32 v114, v159, v115, vcc
	v_cmp_ne_u32_e32 vcc, 30, v66
	s_nop 1
	v_cndmask_b32_e32 v115, v159, v116, vcc
	v_cmp_ne_u32_e32 vcc, 31, v66
	s_nop 1
	v_cndmask_b32_e32 v116, v159, v117, vcc
	v_cmp_gt_f32_e32 vcc, v69, v67
	s_nop 1
	v_cndmask_b32_e32 v67, v67, v69, vcc
	v_cndmask_b32_e64 v117, 0, 1, vcc
	v_cmp_gt_f32_e32 vcc, v70, v67
	s_nop 1
	v_cndmask_b32_e32 v67, v67, v70, vcc
	v_cndmask_b32_e64 v117, v117, 2, vcc
	v_cmp_gt_f32_e32 vcc, v71, v67
	s_nop 1
	v_cndmask_b32_e32 v67, v67, v71, vcc
	v_cndmask_b32_e64 v117, v117, 3, vcc
	v_cmp_gt_f32_e32 vcc, v72, v67
	s_nop 1
	v_cndmask_b32_e32 v67, v67, v72, vcc
	v_cndmask_b32_e64 v117, v117, 4, vcc
	v_cmp_gt_f32_e32 vcc, v90, v67
	s_nop 1
	v_cndmask_b32_e32 v67, v67, v90, vcc
	v_cndmask_b32_e64 v117, v117, 5, vcc
	v_cmp_gt_f32_e32 vcc, v91, v67
	s_nop 1
	v_cndmask_b32_e32 v67, v67, v91, vcc
	v_cndmask_b32_e64 v117, v117, 6, vcc
	v_cmp_gt_f32_e32 vcc, v92, v67
	s_nop 1
	v_cndmask_b32_e32 v67, v67, v92, vcc
	v_cndmask_b32_e64 v117, v117, 7, vcc
	v_cmp_gt_f32_e32 vcc, v93, v67
	s_nop 1
	v_cndmask_b32_e32 v67, v67, v93, vcc
	v_cndmask_b32_e64 v117, v117, 8, vcc
	v_cmp_gt_f32_e32 vcc, v94, v67
	s_nop 1
	v_cndmask_b32_e32 v67, v67, v94, vcc
	v_cndmask_b32_e64 v117, v117, 9, vcc
	v_cmp_gt_f32_e32 vcc, v95, v67
	s_nop 1
	v_cndmask_b32_e32 v67, v67, v95, vcc
	v_cndmask_b32_e64 v117, v117, 10, vcc
	v_cmp_gt_f32_e32 vcc, v96, v67
	s_nop 1
	v_cndmask_b32_e32 v67, v67, v96, vcc
	v_cndmask_b32_e64 v117, v117, 11, vcc
	v_cmp_gt_f32_e32 vcc, v97, v67
	s_nop 1
	v_cndmask_b32_e32 v67, v67, v97, vcc
	v_cndmask_b32_e64 v117, v117, 12, vcc
	v_cmp_gt_f32_e32 vcc, v98, v67
	s_nop 1
	v_cndmask_b32_e32 v67, v67, v98, vcc
	v_cndmask_b32_e64 v117, v117, 13, vcc
	v_cmp_gt_f32_e32 vcc, v99, v67
	s_nop 1
	v_cndmask_b32_e32 v67, v67, v99, vcc
	v_cndmask_b32_e64 v117, v117, 14, vcc
	v_cmp_gt_f32_e32 vcc, v100, v67
	s_nop 1
	v_cndmask_b32_e32 v67, v67, v100, vcc
	v_cndmask_b32_e64 v117, v117, 15, vcc
	v_cmp_gt_f32_e32 vcc, v101, v67
	s_nop 1
	v_cndmask_b32_e32 v67, v67, v101, vcc
	v_cndmask_b32_e64 v117, v117, 16, vcc
	v_cmp_gt_f32_e32 vcc, v102, v67
	s_nop 1
	v_cndmask_b32_e32 v67, v67, v102, vcc
	v_cndmask_b32_e64 v117, v117, 17, vcc
	v_cmp_gt_f32_e32 vcc, v103, v67
	s_nop 1
	v_cndmask_b32_e32 v67, v67, v103, vcc
	v_cndmask_b32_e64 v117, v117, 18, vcc
	v_cmp_gt_f32_e32 vcc, v104, v67
	s_nop 1
	v_cndmask_b32_e32 v67, v67, v104, vcc
	v_cndmask_b32_e64 v117, v117, 19, vcc
	v_cmp_gt_f32_e32 vcc, v105, v67
	s_nop 1
	v_cndmask_b32_e32 v67, v67, v105, vcc
	v_cndmask_b32_e64 v117, v117, 20, vcc
	v_cmp_gt_f32_e32 vcc, v106, v67
	s_nop 1
	v_cndmask_b32_e32 v67, v67, v106, vcc
	v_cndmask_b32_e64 v117, v117, 21, vcc
	v_cmp_gt_f32_e32 vcc, v107, v67
	s_nop 1
	v_cndmask_b32_e32 v67, v67, v107, vcc
	v_cndmask_b32_e64 v117, v117, 22, vcc
	v_cmp_gt_f32_e32 vcc, v108, v67
	s_nop 1
	v_cndmask_b32_e32 v67, v67, v108, vcc
	v_cndmask_b32_e64 v117, v117, 23, vcc
	v_cmp_gt_f32_e32 vcc, v109, v67
	s_nop 1
	v_cndmask_b32_e32 v67, v67, v109, vcc
	v_cndmask_b32_e64 v117, v117, 24, vcc
	v_cmp_gt_f32_e32 vcc, v110, v67
	s_nop 1
	v_cndmask_b32_e32 v67, v67, v110, vcc
	v_cndmask_b32_e64 v117, v117, 25, vcc
	v_cmp_gt_f32_e32 vcc, v111, v67
	s_nop 1
	v_cndmask_b32_e32 v67, v67, v111, vcc
	v_cndmask_b32_e64 v117, v117, 26, vcc
	v_cmp_gt_f32_e32 vcc, v112, v67
	s_nop 1
	v_cndmask_b32_e32 v67, v67, v112, vcc
	v_cndmask_b32_e64 v117, v117, 27, vcc
	v_cmp_gt_f32_e32 vcc, v113, v67
	s_nop 1
	v_cndmask_b32_e32 v67, v67, v113, vcc
	v_cndmask_b32_e64 v117, v117, 28, vcc
	v_cmp_gt_f32_e32 vcc, v114, v67
	s_nop 1
	v_cndmask_b32_e32 v67, v67, v114, vcc
	v_cndmask_b32_e64 v117, v117, 29, vcc
	v_cmp_gt_f32_e32 vcc, v115, v67
	s_nop 1
	v_cndmask_b32_e32 v118, v67, v115, vcc
	v_cndmask_b32_e64 v117, v117, 30, vcc
	v_cmp_gt_f32_e32 vcc, v116, v118
	s_nop 1
	v_cndmask_b32_e64 v67, v117, 31, vcc
	v_cndmask_b32_e32 v117, v118, v116, vcc
	v_cmp_ne_u32_e32 vcc, 0, v67
	s_nop 1
	v_cndmask_b32_e32 v118, v159, v68, vcc
	v_cmp_ne_u32_e32 vcc, 1, v67
	v_max_f32_e32 v68, v118, v118
	v_max_f32_e32 v68, 0xff7fc99e, v68
	v_cndmask_b32_e32 v69, v159, v69, vcc
	v_cmp_ne_u32_e32 vcc, 2, v67
	s_nop 1
	v_cndmask_b32_e32 v70, v159, v70, vcc
	v_cmp_ne_u32_e32 vcc, 3, v67
	s_nop 1
	v_cndmask_b32_e32 v71, v159, v71, vcc
	v_cmp_ne_u32_e32 vcc, 4, v67
	s_nop 1
	v_cndmask_b32_e32 v72, v159, v72, vcc
	v_cmp_ne_u32_e32 vcc, 5, v67
	s_nop 1
	v_cndmask_b32_e32 v90, v159, v90, vcc
	v_cmp_ne_u32_e32 vcc, 6, v67
	s_nop 1
	v_cndmask_b32_e32 v91, v159, v91, vcc
	v_cmp_ne_u32_e32 vcc, 7, v67
	s_nop 1
	v_cndmask_b32_e32 v92, v159, v92, vcc
	v_cmp_ne_u32_e32 vcc, 8, v67
	s_nop 1
	v_cndmask_b32_e32 v93, v159, v93, vcc
; template <bool SKIP_MIX>
; __device__ __forceinline__ void p8_ln_router(Frame& F0, const In& I) {
;     ...
;             for (int k = 0; k < 4; ++k) { float best = -3.4e38f; int bi = 0;
; #pragma unroll
;                 for (int e = 0; e < 32; ++e) { const bool tk = lv[e] > best; best = tk ? lv[e] : best; bi = tk ? e : bi; }
;                 ti[k] = bi; tv[k] = best;
; #pragma unroll
;                 for (int e = 0; e < 32; ++e) lv[e] = (e == bi) ? -3.4e38f : lv[e]; }
	v_cmp_ne_u32_e32 vcc, 9, v67
	s_nop 1
	v_cndmask_b32_e32 v94, v159, v94, vcc
	v_cmp_ne_u32_e32 vcc, 10, v67
	s_nop 1
	v_cndmask_b32_e32 v95, v159, v95, vcc
	v_cmp_ne_u32_e32 vcc, 11, v67
	s_nop 1
	v_cndmask_b32_e32 v96, v159, v96, vcc
	v_cmp_ne_u32_e32 vcc, 12, v67
	s_nop 1
	v_cndmask_b32_e32 v97, v159, v97, vcc
	v_cmp_ne_u32_e32 vcc, 13, v67
	s_nop 1
	v_cndmask_b32_e32 v98, v159, v98, vcc
	v_cmp_ne_u32_e32 vcc, 14, v67
	s_nop 1
	v_cndmask_b32_e32 v99, v159, v99, vcc
	v_cmp_ne_u32_e32 vcc, 15, v67
	s_nop 1
	v_cndmask_b32_e32 v100, v159, v100, vcc
	v_cmp_ne_u32_e32 vcc, 16, v67
	s_nop 1
	v_cndmask_b32_e32 v101, v159, v101, vcc
	v_cmp_ne_u32_e32 vcc, 17, v67
	s_nop 1
	v_cndmask_b32_e32 v102, v159, v102, vcc
	v_cmp_ne_u32_e32 vcc, 18, v67
	s_nop 1
	v_cndmask_b32_e32 v103, v159, v103, vcc
	v_cmp_ne_u32_e32 vcc, 19, v67
	s_nop 1
	v_cndmask_b32_e32 v104, v159, v104, vcc
	v_cmp_ne_u32_e32 vcc, 20, v67
	s_nop 1
	v_cndmask_b32_e32 v105, v159, v105, vcc
	v_cmp_ne_u32_e32 vcc, 21, v67
	s_nop 1
	v_cndmask_b32_e32 v106, v159, v106, vcc
	v_cmp_ne_u32_e32 vcc, 22, v67
	s_nop 1
	v_cndmask_b32_e32 v107, v159, v107, vcc
	v_cmp_ne_u32_e32 vcc, 23, v67
	s_nop 1
	v_cndmask_b32_e32 v108, v159, v108, vcc
	v_cmp_ne_u32_e32 vcc, 24, v67
	s_nop 1
	v_cndmask_b32_e32 v109, v159, v109, vcc
	v_cmp_ne_u32_e32 vcc, 25, v67
	s_nop 1
	v_cndmask_b32_e32 v110, v159, v110, vcc
	v_cmp_ne_u32_e32 vcc, 26, v67
	s_nop 1
	v_cndmask_b32_e32 v111, v159, v111, vcc
	v_cmp_ne_u32_e32 vcc, 27, v67
	s_nop 1
	v_cndmask_b32_e32 v112, v159, v112, vcc
	v_cmp_ne_u32_e32 vcc, 28, v67
	s_nop 1
	v_cndmask_b32_e32 v113, v159, v113, vcc
	v_cmp_ne_u32_e32 vcc, 29, v67
	s_nop 1
	v_cndmask_b32_e32 v114, v159, v114, vcc
	v_cmp_ne_u32_e32 vcc, 30, v67
	s_nop 1
	v_cndmask_b32_e32 v115, v159, v115, vcc
	v_cmp_ne_u32_e32 vcc, 31, v67
	s_nop 1
	v_cndmask_b32_e32 v116, v159, v116, vcc
	v_cmp_gt_f32_e32 vcc, v69, v68
	s_nop 1
	v_cndmask_b32_e32 v68, v68, v69, vcc
	v_cndmask_b32_e64 v119, 0, 1, vcc
	v_cmp_gt_f32_e32 vcc, v70, v68
	s_nop 1
	v_cndmask_b32_e32 v68, v68, v70, vcc
	v_cndmask_b32_e64 v119, v119, 2, vcc
	v_cmp_gt_f32_e32 vcc, v71, v68
	s_nop 1
	v_cndmask_b32_e32 v68, v68, v71, vcc
	v_cndmask_b32_e64 v119, v119, 3, vcc
	v_cmp_gt_f32_e32 vcc, v72, v68
	s_nop 1
	v_cndmask_b32_e32 v68, v68, v72, vcc
	v_cndmask_b32_e64 v119, v119, 4, vcc
	v_cmp_gt_f32_e32 vcc, v90, v68
	s_nop 1
	v_cndmask_b32_e32 v68, v68, v90, vcc
	v_cndmask_b32_e64 v119, v119, 5, vcc
	v_cmp_gt_f32_e32 vcc, v91, v68
	s_nop 1
	v_cndmask_b32_e32 v68, v68, v91, vcc
	v_cndmask_b32_e64 v119, v119, 6, vcc
	v_cmp_gt_f32_e32 vcc, v92, v68
	s_nop 1
	v_cndmask_b32_e32 v68, v68, v92, vcc
	v_cndmask_b32_e64 v119, v119, 7, vcc
	v_cmp_gt_f32_e32 vcc, v93, v68
	s_nop 1
	v_cndmask_b32_e32 v68, v68, v93, vcc
	v_cndmask_b32_e64 v119, v119, 8, vcc
	v_cmp_gt_f32_e32 vcc, v94, v68
	s_nop 1
	v_cndmask_b32_e32 v68, v68, v94, vcc
	v_cndmask_b32_e64 v119, v119, 9, vcc
	v_cmp_gt_f32_e32 vcc, v95, v68
	s_nop 1
	v_cndmask_b32_e32 v68, v68, v95, vcc
	v_cndmask_b32_e64 v119, v119, 10, vcc
	v_cmp_gt_f32_e32 vcc, v96, v68
	s_nop 1
	v_cndmask_b32_e32 v68, v68, v96, vcc
	v_cndmask_b32_e64 v119, v119, 11, vcc
	v_cmp_gt_f32_e32 vcc, v97, v68
	s_nop 1
	v_cndmask_b32_e32 v68, v68, v97, vcc
	v_cndmask_b32_e64 v119, v119, 12, vcc
	v_cmp_gt_f32_e32 vcc, v98, v68
	s_nop 1
	v_cndmask_b32_e32 v68, v68, v98, vcc
	v_cndmask_b32_e64 v119, v119, 13, vcc
	v_cmp_gt_f32_e32 vcc, v99, v68
	s_nop 1
	v_cndmask_b32_e32 v68, v68, v99, vcc
	v_cndmask_b32_e64 v119, v119, 14, vcc
	v_cmp_gt_f32_e32 vcc, v100, v68
	s_nop 1
	v_cndmask_b32_e32 v68, v68, v100, vcc
	v_cndmask_b32_e64 v119, v119, 15, vcc
	v_cmp_gt_f32_e32 vcc, v101, v68
	s_nop 1
	v_cndmask_b32_e32 v68, v68, v101, vcc
	v_cndmask_b32_e64 v119, v119, 16, vcc
	v_cmp_gt_f32_e32 vcc, v102, v68
	s_nop 1
	v_cndmask_b32_e32 v68, v68, v102, vcc
	v_cndmask_b32_e64 v119, v119, 17, vcc
	v_cmp_gt_f32_e32 vcc, v103, v68
	s_nop 1
	v_cndmask_b32_e32 v68, v68, v103, vcc
	v_cndmask_b32_e64 v119, v119, 18, vcc
	v_cmp_gt_f32_e32 vcc, v104, v68
	s_nop 1
	v_cndmask_b32_e32 v68, v68, v104, vcc
	v_cndmask_b32_e64 v119, v119, 19, vcc
	v_cmp_gt_f32_e32 vcc, v105, v68
	s_nop 1
	v_cndmask_b32_e32 v68, v68, v105, vcc
	v_cndmask_b32_e64 v119, v119, 20, vcc
	v_cmp_gt_f32_e32 vcc, v106, v68
	s_nop 1
	v_cndmask_b32_e32 v68, v68, v106, vcc
	v_cndmask_b32_e64 v119, v119, 21, vcc
	v_cmp_gt_f32_e32 vcc, v107, v68
	s_nop 1
	v_cndmask_b32_e32 v68, v68, v107, vcc
	v_cndmask_b32_e64 v119, v119, 22, vcc
	v_cmp_gt_f32_e32 vcc, v108, v68
	s_nop 1
	v_cndmask_b32_e32 v68, v68, v108, vcc
	v_cndmask_b32_e64 v119, v119, 23, vcc
	v_cmp_gt_f32_e32 vcc, v109, v68
	s_nop 1
	v_cndmask_b32_e32 v68, v68, v109, vcc
	v_cndmask_b32_e64 v119, v119, 24, vcc
	v_cmp_gt_f32_e32 vcc, v110, v68
	s_nop 1
	v_cndmask_b32_e32 v68, v68, v110, vcc
	v_cndmask_b32_e64 v119, v119, 25, vcc
	v_cmp_gt_f32_e32 vcc, v111, v68
	s_nop 1
	v_cndmask_b32_e32 v68, v68, v111, vcc
	v_cndmask_b32_e64 v119, v119, 26, vcc
	v_cmp_gt_f32_e32 vcc, v112, v68
	s_nop 1
	v_cndmask_b32_e32 v68, v68, v112, vcc
	v_cndmask_b32_e64 v119, v119, 27, vcc
	v_cmp_gt_f32_e32 vcc, v113, v68
	s_nop 1
	v_cndmask_b32_e32 v68, v68, v113, vcc
	v_cndmask_b32_e64 v119, v119, 28, vcc
	v_cmp_gt_f32_e32 vcc, v114, v68
	s_nop 1
	v_cndmask_b32_e32 v68, v68, v114, vcc
	v_cndmask_b32_e64 v119, v119, 29, vcc
	v_cmp_gt_f32_e32 vcc, v115, v68
	s_nop 1
	v_cndmask_b32_e32 v120, v68, v115, vcc
	v_cndmask_b32_e64 v119, v119, 30, vcc
	v_cmp_gt_f32_e32 vcc, v116, v120
	s_nop 1
	v_cndmask_b32_e64 v68, v119, 31, vcc
	v_cndmask_b32_e32 v119, v120, v116, vcc
	v_cmp_ne_u32_e32 vcc, 0, v68
	s_nop 1
	v_cndmask_b32_e32 v118, v159, v118, vcc
	v_cmp_ne_u32_e32 vcc, 1, v68
; template <bool SKIP_MIX>
; __device__ __forceinline__ void p8_ln_router(Frame& F0, const In& I) {
;     ...
;             for (int k = 0; k < 4; ++k) { float best = -3.4e38f; int bi = 0;
; #pragma unroll
;                 for (int e = 0; e < 32; ++e) { const bool tk = lv[e] > best; best = tk ? lv[e] : best; bi = tk ? e : bi; }
;                 ti[k] = bi; tv[k] = best;
; #pragma unroll
;                 for (int e = 0; e < 32; ++e) lv[e] = (e == bi) ? -3.4e38f : lv[e]; }
;             float ex[4], sum = 0.f;
; #pragma unroll
;             for (int k = 0; k < 4; ++k) { ex[k] = __expf(tv[k] - tv[0]); sum += ex[k]; }
	v_max_f32_e32 v118, v118, v118
	v_max_f32_e32 v118, 0xff7fc99e, v118
	v_cndmask_b32_e32 v69, v159, v69, vcc
	v_cmp_ne_u32_e32 vcc, 2, v68
	s_nop 1
	v_cndmask_b32_e32 v70, v159, v70, vcc
	v_cmp_ne_u32_e32 vcc, 3, v68
	s_nop 1
	v_cndmask_b32_e32 v71, v159, v71, vcc
	v_cmp_ne_u32_e32 vcc, 4, v68
	s_nop 1
	v_cndmask_b32_e32 v72, v159, v72, vcc
	v_cmp_ne_u32_e32 vcc, 5, v68
	s_nop 1
	v_cndmask_b32_e32 v90, v159, v90, vcc
	v_cmp_ne_u32_e32 vcc, 6, v68
	s_nop 1
	v_cndmask_b32_e32 v91, v159, v91, vcc
	v_cmp_ne_u32_e32 vcc, 7, v68
	s_nop 1
	v_cndmask_b32_e32 v92, v159, v92, vcc
	v_cmp_ne_u32_e32 vcc, 8, v68
	s_nop 1
	v_cndmask_b32_e32 v93, v159, v93, vcc
	v_cmp_ne_u32_e32 vcc, 9, v68
	s_nop 1
	v_cndmask_b32_e32 v94, v159, v94, vcc
	v_cmp_ne_u32_e32 vcc, 10, v68
	s_nop 1
	v_cndmask_b32_e32 v95, v159, v95, vcc
	v_cmp_ne_u32_e32 vcc, 11, v68
	s_nop 1
	v_cndmask_b32_e32 v96, v159, v96, vcc
	v_cmp_ne_u32_e32 vcc, 12, v68
	s_nop 1
	v_cndmask_b32_e32 v97, v159, v97, vcc
	v_cmp_ne_u32_e32 vcc, 13, v68
	s_nop 1
	v_cndmask_b32_e32 v98, v159, v98, vcc
	v_cmp_ne_u32_e32 vcc, 14, v68
	s_nop 1
	v_cndmask_b32_e32 v99, v159, v99, vcc
	v_cmp_ne_u32_e32 vcc, 15, v68
	s_nop 1
	v_cndmask_b32_e32 v100, v159, v100, vcc
	v_cmp_ne_u32_e32 vcc, 16, v68
	s_nop 1
	v_cndmask_b32_e32 v101, v159, v101, vcc
	v_cmp_ne_u32_e32 vcc, 17, v68
	s_nop 1
	v_cndmask_b32_e32 v102, v159, v102, vcc
	v_cmp_ne_u32_e32 vcc, 18, v68
	s_nop 1
	v_cndmask_b32_e32 v103, v159, v103, vcc
	v_cmp_ne_u32_e32 vcc, 19, v68
	s_nop 1
	v_cndmask_b32_e32 v104, v159, v104, vcc
	v_cmp_ne_u32_e32 vcc, 20, v68
	s_nop 1
	v_cndmask_b32_e32 v105, v159, v105, vcc
	v_cmp_ne_u32_e32 vcc, 21, v68
	s_nop 1
	v_cndmask_b32_e32 v106, v159, v106, vcc
	v_cmp_ne_u32_e32 vcc, 22, v68
	s_nop 1
	v_cndmask_b32_e32 v107, v159, v107, vcc
	v_cmp_ne_u32_e32 vcc, 23, v68
	s_nop 1
	v_cndmask_b32_e32 v108, v159, v108, vcc
	v_cmp_ne_u32_e32 vcc, 24, v68
	s_nop 1
	v_cndmask_b32_e32 v109, v159, v109, vcc
	v_cmp_ne_u32_e32 vcc, 25, v68
	s_nop 1
	v_cndmask_b32_e32 v110, v159, v110, vcc
	v_cmp_ne_u32_e32 vcc, 26, v68
	s_nop 1
	v_cndmask_b32_e32 v111, v159, v111, vcc
	v_cmp_ne_u32_e32 vcc, 27, v68
	s_nop 1
	v_cndmask_b32_e32 v112, v159, v112, vcc
	v_cmp_ne_u32_e32 vcc, 28, v68
	s_nop 1
	v_cndmask_b32_e32 v113, v159, v113, vcc
	v_cmp_ne_u32_e32 vcc, 29, v68
	s_nop 1
	v_cndmask_b32_e32 v114, v159, v114, vcc
	v_cmp_ne_u32_e32 vcc, 30, v68
	s_nop 1
	v_cndmask_b32_e32 v115, v159, v115, vcc
	v_cmp_ne_u32_e32 vcc, 31, v68
	s_nop 1
	v_cndmask_b32_e32 v116, v159, v116, vcc
	v_cmp_gt_f32_e32 vcc, v69, v118
	s_nop 1
	v_cndmask_b32_e32 v69, v118, v69, vcc
	v_cndmask_b32_e64 v120, 0, 1, vcc
	v_cmp_gt_f32_e32 vcc, v70, v69
	s_nop 1
	v_cndmask_b32_e32 v69, v69, v70, vcc
	v_cndmask_b32_e64 v118, v120, 2, vcc
	v_cmp_gt_f32_e32 vcc, v71, v69
	s_nop 1
	v_cndmask_b32_e32 v69, v69, v71, vcc
	v_cndmask_b32_e64 v70, v118, 3, vcc
	v_cmp_gt_f32_e32 vcc, v72, v69
	s_nop 1
	v_cndmask_b32_e32 v69, v69, v72, vcc
	v_cndmask_b32_e64 v70, v70, 4, vcc
	v_cmp_gt_f32_e32 vcc, v90, v69
	v_sub_f32_e32 v72, v119, v73
	v_mul_f32_e32 v72, 0x3fb8aa3b, v72
	v_cndmask_b32_e32 v69, v69, v90, vcc
	v_cndmask_b32_e64 v70, v70, 5, vcc
	v_cmp_gt_f32_e32 vcc, v91, v69
	v_exp_f32_e32 v72, v72
	s_nop 0
	v_cndmask_b32_e32 v69, v69, v91, vcc
	v_cndmask_b32_e64 v70, v70, 6, vcc
	v_cmp_gt_f32_e32 vcc, v92, v69
	s_nop 1
	v_cndmask_b32_e32 v69, v69, v92, vcc
	v_cndmask_b32_e64 v70, v70, 7, vcc
	v_cmp_gt_f32_e32 vcc, v93, v69
	s_nop 1
	v_cndmask_b32_e32 v69, v69, v93, vcc
	v_cndmask_b32_e64 v70, v70, 8, vcc
	v_cmp_gt_f32_e32 vcc, v94, v69
	s_nop 1
	v_cndmask_b32_e32 v69, v69, v94, vcc
	v_cndmask_b32_e64 v70, v70, 9, vcc
	v_cmp_gt_f32_e32 vcc, v95, v69
	s_nop 1
	v_cndmask_b32_e32 v69, v69, v95, vcc
	v_cndmask_b32_e64 v70, v70, 10, vcc
	v_cmp_gt_f32_e32 vcc, v96, v69
	s_nop 1
	v_cndmask_b32_e32 v69, v69, v96, vcc
; #define GAS __attribute__((address_space(1)))
; template <bool SKIP_MIX>
; __device__ __forceinline__ void p8_ln_router(Frame& F0, const In& I) {
;     ...
;             float ex[4], sum = 0.f;
; #pragma unroll
;             for (int k = 0; k < 4; ++k) { ex[k] = __expf(tv[k] - tv[0]); sum += ex[k]; }
;             const float inv = 1.f / sum;
;             *(GAS v4u*)((int*)(F.ws + WS_TOPI) + (size_t)(tok0 + tl) * 4) = (v4u){(unsigned)ti[0], (unsigned)ti[1], (unsigned)ti[2], (unsigned)ti[3]};
;             *(GAS f32x4*)((float*)(F.ws + WS_GATE) + (size_t)(tok0 + tl) * 4) = (f32x4){ex[0] * inv, ex[1] * inv, ex[2] * inv, ex[3] * inv};
; #pragma unroll
;             for (int k = 0; k < 4; ++k) __hip_atomic_fetch_add(&hist[ti[k]], 1, __ATOMIC_RELAXED, __HIP_MEMORY_SCOPE_WORKGROUP);
;         }
;         __syncthreads();
	v_cndmask_b32_e64 v70, v70, 11, vcc
	v_cmp_gt_f32_e32 vcc, v97, v69
	s_nop 1
	v_cndmask_b32_e32 v69, v69, v97, vcc
	v_cndmask_b32_e64 v70, v70, 12, vcc
	v_cmp_gt_f32_e32 vcc, v98, v69
	s_nop 1
	v_cndmask_b32_e32 v69, v69, v98, vcc
	v_cndmask_b32_e64 v70, v70, 13, vcc
	v_cmp_gt_f32_e32 vcc, v99, v69
	s_nop 1
	v_cndmask_b32_e32 v69, v69, v99, vcc
	v_cndmask_b32_e64 v70, v70, 14, vcc
	v_cmp_gt_f32_e32 vcc, v100, v69
	s_nop 1
	v_cndmask_b32_e32 v69, v69, v100, vcc
	v_cndmask_b32_e64 v70, v70, 15, vcc
	v_cmp_gt_f32_e32 vcc, v101, v69
	s_nop 1
	v_cndmask_b32_e32 v69, v69, v101, vcc
	v_cndmask_b32_e64 v70, v70, 16, vcc
	v_cmp_gt_f32_e32 vcc, v102, v69
	s_nop 1
	v_cndmask_b32_e32 v69, v69, v102, vcc
	v_cndmask_b32_e64 v70, v70, 17, vcc
	v_cmp_gt_f32_e32 vcc, v103, v69
	s_nop 1
	v_cndmask_b32_e32 v69, v69, v103, vcc
	v_cndmask_b32_e64 v70, v70, 18, vcc
	v_cmp_gt_f32_e32 vcc, v104, v69
	s_nop 1
	v_cndmask_b32_e32 v69, v69, v104, vcc
	v_cndmask_b32_e64 v70, v70, 19, vcc
	v_cmp_gt_f32_e32 vcc, v105, v69
	s_nop 1
	v_cndmask_b32_e32 v69, v69, v105, vcc
	v_cndmask_b32_e64 v70, v70, 20, vcc
	v_cmp_gt_f32_e32 vcc, v106, v69
	s_nop 1
	v_cndmask_b32_e32 v69, v69, v106, vcc
	v_cndmask_b32_e64 v70, v70, 21, vcc
	v_cmp_gt_f32_e32 vcc, v107, v69
	s_nop 1
	v_cndmask_b32_e32 v69, v69, v107, vcc
	v_cndmask_b32_e64 v70, v70, 22, vcc
	v_cmp_gt_f32_e32 vcc, v108, v69
	s_nop 1
	v_cndmask_b32_e32 v69, v69, v108, vcc
	v_cndmask_b32_e64 v70, v70, 23, vcc
	v_cmp_gt_f32_e32 vcc, v109, v69
	s_nop 1
	v_cndmask_b32_e32 v69, v69, v109, vcc
	v_cndmask_b32_e64 v70, v70, 24, vcc
	v_cmp_gt_f32_e32 vcc, v110, v69
	s_nop 1
	v_cndmask_b32_e32 v69, v69, v110, vcc
	v_cndmask_b32_e64 v70, v70, 25, vcc
	v_cmp_gt_f32_e32 vcc, v111, v69
	s_nop 1
	v_cndmask_b32_e32 v69, v69, v111, vcc
	v_cndmask_b32_e64 v70, v70, 26, vcc
	v_cmp_gt_f32_e32 vcc, v112, v69
	s_nop 1
	v_cndmask_b32_e32 v69, v69, v112, vcc
	v_cndmask_b32_e64 v70, v70, 27, vcc
	v_cmp_gt_f32_e32 vcc, v113, v69
	s_nop 1
	v_cndmask_b32_e32 v69, v69, v113, vcc
	v_cndmask_b32_e64 v70, v70, 28, vcc
	v_cmp_gt_f32_e32 vcc, v114, v69
	s_nop 1
	v_cndmask_b32_e32 v69, v69, v114, vcc
	v_cndmask_b32_e64 v70, v70, 29, vcc
	v_cmp_gt_f32_e32 vcc, v115, v69
	s_nop 1
	v_cndmask_b32_e32 v71, v69, v115, vcc
	v_cndmask_b32_e64 v70, v70, 30, vcc
	v_cmp_gt_f32_e32 vcc, v116, v71
	s_nop 1
	v_cndmask_b32_e64 v69, v70, 31, vcc
	v_sub_f32_e32 v70, v73, v73
	v_cndmask_b32_e32 v90, v71, v116, vcc
	v_mul_f32_e32 v70, 0x3fb8aa3b, v70
	v_sub_f32_e32 v71, v117, v73
	v_exp_f32_e32 v70, v70
	v_mul_f32_e32 v71, 0x3fb8aa3b, v71
	v_exp_f32_e32 v71, v71
	v_sub_f32_e32 v73, v90, v73
	v_mul_f32_e32 v73, 0x3fb8aa3b, v73
	v_exp_f32_e32 v73, v73
	v_add_f32_e32 v90, 0, v70
	v_add_f32_e32 v90, v90, v71
	v_add_f32_e32 v90, v90, v72
	v_add_f32_e32 v90, v90, v73
	v_div_scale_f32 v91, s[14:15], v90, v90, 1.0
	v_rcp_f32_e32 v92, v91
	s_nop 0
	v_fma_f32 v93, -v91, v92, 1.0
	v_fmac_f32_e32 v92, v93, v92
	v_div_scale_f32 v93, vcc, 1.0, v90, 1.0
	v_mul_f32_e32 v94, v93, v92
	v_fma_f32 v95, -v91, v94, v93
	v_fmac_f32_e32 v94, v95, v92
	v_fma_f32 v91, -v91, v94, v93
	v_div_fmas_f32 v91, v91, v92, v94
	v_add_u32_e32 v92, s23, v74
	v_ashrrev_i32_e32 v93, 31, v92
	v_div_fixup_f32 v90, v91, v90, 1.0
	v_lshlrev_b64 v[92:93], 4, v[92:93]
	v_lshl_add_u64 v[94:95], s[6:7], 0, v[92:93]
	v_pk_mul_f32 v[72:73], v[72:73], v[90:91] op_sel_hi:[1,0]
	v_pk_mul_f32 v[70:71], v[70:71], v[90:91] op_sel_hi:[1,0]
	v_lshl_add_u64 v[90:91], s[10:11], 0, v[92:93]
	global_store_dwordx4 v[94:95], v[66:69], off
	global_store_dwordx4 v[90:91], v[70:73], off
	s_nop 0
	v_lshl_add_u32 v66, v66, 2, s21
	ds_add_u32 v66, v158
	v_lshl_add_u32 v66, v67, 2, s21
	ds_add_u32 v66, v158
	v_lshl_add_u32 v66, v68, 2, s21
	ds_add_u32 v66, v158
	v_lshl_add_u32 v66, v69, 2, s21
	ds_add_u32 v66, v158
	s_branch .LBB0_1513
